# hand-scheduled RWKV-7 recurrence chunk body with 2-step LDS operand prefetch; LDS-DMA issue interleaved with ds_reads in all GEMM K-loop load segments
# speedup vs baseline: 1.0060x; 1.0033x over previous
.LBB0_187:
	s_cmp_eq_u32 s25, 28
	v_lshl_add_u64 v[204:205], v[156:157], 0, s[20:21]
	s_cselect_b64 vcc, -1, 0
	v_cndmask_b32_e32 v237, v205, v153, vcc
	v_cndmask_b32_e32 v236, v204, v152, vcc
	v_cndmask_b32_e32 v239, v159, v155, vcc
	v_cndmask_b32_e32 v238, v158, v154, vcc
	s_mov_b32 m0, s40
	v_lshl_add_u64 v[240:241], v[156:157], 0, v[138:139]
	global_load_lds_dwordx4 v[240:241], off
	ds_read_b128 v[172:175], v166
	ds_read_b128 v[176:179], v166 offset:1024
	ds_read_b128 v[180:183], v166 offset:2048
	ds_read_b128 v[184:187], v166 offset:3072
	ds_read_b128 v[188:191], v167
	ds_read_b128 v[192:195], v167 offset:1024
	v_lshl_add_u64 v[240:241], v[156:157], 0, v[140:141]
	s_mov_b32 m0, s41
	s_nop 0
	global_load_lds_dwordx4 v[240:241], off
	ds_read_b128 v[196:199], v167 offset:2048
	ds_read_b128 v[200:203], v167 offset:3072
	ds_read_b128 v[204:207], v168
	ds_read_b128 v[208:211], v168 offset:1024
	ds_read_b128 v[212:215], v168 offset:2048
	ds_read_b128 v[216:219], v168 offset:3072
	ds_read_b128 v[220:223], v168 offset:4096
	ds_read_b128 v[224:227], v168 offset:5120
	ds_read_b128 v[228:231], v168 offset:6144
	ds_read_b128 v[232:235], v168 offset:7168
	s_waitcnt vmcnt(8)
	s_waitcnt lgkmcnt(0)
	s_barrier
	s_setprio 1
	s_waitcnt lgkmcnt(0)
	v_mfma_f32_16x16x32_bf16 v[124:127], v[172:175], v[204:207], v[124:127]
	v_mfma_f32_16x16x32_bf16 v[120:123], v[180:183], v[204:207], v[120:123]
	v_mfma_f32_16x16x32_bf16 v[116:119], v[172:175], v[212:215], v[116:119]
	v_mfma_f32_16x16x32_bf16 v[112:115], v[180:183], v[212:215], v[112:115]
	v_mfma_f32_16x16x32_bf16 v[100:103], v[172:175], v[220:223], v[100:103]
	v_mfma_f32_16x16x32_bf16 v[96:99], v[180:183], v[220:223], v[96:99]
	v_mfma_f32_16x16x32_bf16 v[84:87], v[172:175], v[228:231], v[84:87]
	v_mfma_f32_16x16x32_bf16 v[80:83], v[180:183], v[228:231], v[80:83]
	v_mfma_f32_16x16x32_bf16 v[124:127], v[176:179], v[208:211], v[124:127]
	v_mfma_f32_16x16x32_bf16 v[120:123], v[184:187], v[208:211], v[120:123]
	v_mfma_f32_16x16x32_bf16 v[116:119], v[176:179], v[216:219], v[116:119]
	v_mfma_f32_16x16x32_bf16 v[112:115], v[184:187], v[216:219], v[112:115]
	v_mfma_f32_16x16x32_bf16 v[100:103], v[176:179], v[224:227], v[100:103]
	v_mfma_f32_16x16x32_bf16 v[96:99], v[184:187], v[224:227], v[96:99]
	v_mfma_f32_16x16x32_bf16 v[84:87], v[176:179], v[232:235], v[84:87]
	v_mfma_f32_16x16x32_bf16 v[80:83], v[184:187], v[232:235], v[80:83]
	s_setprio 0
	s_setprio 1
	v_mfma_f32_16x16x32_bf16 v[108:111], v[188:191], v[204:207], v[108:111]
	v_mfma_f32_16x16x32_bf16 v[104:107], v[196:199], v[204:207], v[104:107]
	v_mfma_f32_16x16x32_bf16 v[92:95], v[188:191], v[212:215], v[92:95]
	v_mfma_f32_16x16x32_bf16 v[88:91], v[196:199], v[212:215], v[88:91]
	v_mfma_f32_16x16x32_bf16 v[76:79], v[188:191], v[220:223], v[76:79]
	v_mfma_f32_16x16x32_bf16 v[72:75], v[196:199], v[220:223], v[72:75]
	v_mfma_f32_16x16x32_bf16 v[68:71], v[188:191], v[228:231], v[68:71]
	v_mfma_f32_16x16x32_bf16 v[64:67], v[196:199], v[228:231], v[64:67]
	v_mfma_f32_16x16x32_bf16 v[108:111], v[192:195], v[208:211], v[108:111]
	v_mfma_f32_16x16x32_bf16 v[104:107], v[200:203], v[208:211], v[104:107]
	v_mfma_f32_16x16x32_bf16 v[92:95], v[192:195], v[216:219], v[92:95]
	v_mfma_f32_16x16x32_bf16 v[88:91], v[200:203], v[216:219], v[88:91]
	v_mfma_f32_16x16x32_bf16 v[76:79], v[192:195], v[224:227], v[76:79]
	v_mfma_f32_16x16x32_bf16 v[72:75], v[200:203], v[224:227], v[72:75]
	v_mfma_f32_16x16x32_bf16 v[68:71], v[192:195], v[232:235], v[68:71]
	v_mfma_f32_16x16x32_bf16 v[64:67], v[200:203], v[232:235], v[64:67]
	s_setprio 0
	s_barrier
	s_mov_b32 m0, s42
	v_lshl_add_u64 v[240:241], v[238:239], 0, v[134:135]
	global_load_lds_dwordx4 v[240:241], off
	ds_read_b128 v[204:207], v168 offset:16384
	ds_read_b128 v[208:211], v168 offset:17408
	v_lshl_add_u64 v[242:243], v[238:239], 0, v[130:131]
	s_mov_b32 m0, s43
	v_lshl_add_u64 v[244:245], v[238:239], 0, s[6:7]
	global_load_lds_dwordx4 v[242:243], off
	ds_read_b128 v[212:215], v168 offset:18432
	ds_read_b128 v[216:219], v168 offset:19456
	v_lshl_add_u64 v[246:247], v[244:245], 0, v[134:135]
	s_mov_b32 m0, s44
	v_lshl_add_u64 v[244:245], v[244:245], 0, v[130:131]
	global_load_lds_dwordx4 v[246:247], off
	ds_read_b128 v[220:223], v168 offset:20480
	ds_read_b128 v[224:227], v168 offset:21504
	s_mov_b32 m0, s45
	v_lshl_add_u64 v[246:247], v[236:237], 0, v[132:133]
	global_load_lds_dwordx4 v[244:245], off
	ds_read_b128 v[228:231], v168 offset:22528
	ds_read_b128 v[232:235], v168 offset:23552
	v_lshl_add_u64 v[244:245], v[236:237], 0, v[136:137]
	s_mov_b32 m0, s23
	s_nop 0
	global_load_lds_dwordx4 v[244:245], off
	s_mov_b32 m0, s35
	s_nop 0
	global_load_lds_dwordx4 v[246:247], off
	s_waitcnt vmcnt(8)
	s_waitcnt lgkmcnt(0)
	s_barrier
	s_setprio 1
	s_waitcnt lgkmcnt(0)
	v_mfma_f32_16x16x32_bf16 v[60:63], v[172:175], v[204:207], v[60:63]
	v_mfma_f32_16x16x32_bf16 v[56:59], v[180:183], v[204:207], v[56:59]
	v_mfma_f32_16x16x32_bf16 v[52:55], v[172:175], v[212:215], v[52:55]
	v_mfma_f32_16x16x32_bf16 v[48:51], v[180:183], v[212:215], v[48:51]
	v_mfma_f32_16x16x32_bf16 v[36:39], v[172:175], v[220:223], v[36:39]
	v_mfma_f32_16x16x32_bf16 v[32:35], v[180:183], v[220:223], v[32:35]
	v_mfma_f32_16x16x32_bf16 v[20:23], v[172:175], v[228:231], v[20:23]
	v_mfma_f32_16x16x32_bf16 v[16:19], v[180:183], v[228:231], v[16:19]
	v_mfma_f32_16x16x32_bf16 v[60:63], v[176:179], v[208:211], v[60:63]
	v_mfma_f32_16x16x32_bf16 v[56:59], v[184:187], v[208:211], v[56:59]
	v_mfma_f32_16x16x32_bf16 v[52:55], v[176:179], v[216:219], v[52:55]
	v_mfma_f32_16x16x32_bf16 v[48:51], v[184:187], v[216:219], v[48:51]
	v_mfma_f32_16x16x32_bf16 v[36:39], v[176:179], v[224:227], v[36:39]
	v_mfma_f32_16x16x32_bf16 v[32:35], v[184:187], v[224:227], v[32:35]
	v_mfma_f32_16x16x32_bf16 v[20:23], v[176:179], v[232:235], v[20:23]
	v_mfma_f32_16x16x32_bf16 v[16:19], v[184:187], v[232:235], v[16:19]
	s_setprio 0
	s_setprio 1
	v_mfma_f32_16x16x32_bf16 v[44:47], v[188:191], v[204:207], v[44:47]
	v_mfma_f32_16x16x32_bf16 v[40:43], v[196:199], v[204:207], v[40:43]
	v_mfma_f32_16x16x32_bf16 v[28:31], v[188:191], v[212:215], v[28:31]
	v_mfma_f32_16x16x32_bf16 v[24:27], v[196:199], v[212:215], v[24:27]
	v_mfma_f32_16x16x32_bf16 v[12:15], v[188:191], v[220:223], v[12:15]
	v_mfma_f32_16x16x32_bf16 v[8:11], v[196:199], v[220:223], v[8:11]
	v_mfma_f32_16x16x32_bf16 v[4:7], v[188:191], v[228:231], v[4:7]
	v_mfma_f32_16x16x32_bf16 v[0:3], v[196:199], v[228:231], v[0:3]
	v_mfma_f32_16x16x32_bf16 v[44:47], v[192:195], v[208:211], v[44:47]
	v_mfma_f32_16x16x32_bf16 v[40:43], v[200:203], v[208:211], v[40:43]
	v_mfma_f32_16x16x32_bf16 v[28:31], v[192:195], v[216:219], v[28:31]
	v_mfma_f32_16x16x32_bf16 v[24:27], v[200:203], v[216:219], v[24:27]
	v_mfma_f32_16x16x32_bf16 v[12:15], v[192:195], v[224:227], v[12:15]
	v_mfma_f32_16x16x32_bf16 v[8:11], v[200:203], v[224:227], v[8:11]
	v_mfma_f32_16x16x32_bf16 v[4:7], v[192:195], v[232:235], v[4:7]
	v_mfma_f32_16x16x32_bf16 v[0:3], v[200:203], v[232:235], v[0:3]
	s_setprio 0
	s_barrier
	v_lshl_add_u64 v[236:237], v[236:237], 0, s[6:7]
	s_mov_b32 m0, s36
	v_lshl_add_u64 v[248:249], v[236:237], 0, v[136:137]
	global_load_lds_dwordx4 v[248:249], off
	ds_read_b128 v[172:175], v169
	ds_read_b128 v[176:179], v169 offset:1024
	ds_read_b128 v[180:183], v169 offset:2048
	ds_read_b128 v[184:187], v169 offset:3072
	ds_read_b128 v[188:191], v170
	ds_read_b128 v[192:195], v170 offset:1024
	v_lshl_add_u64 v[236:237], v[236:237], 0, v[132:133]
	s_mov_b32 m0, s37
	s_nop 0
	global_load_lds_dwordx4 v[236:237], off
	ds_read_b128 v[196:199], v170 offset:2048
	ds_read_b128 v[200:203], v170 offset:3072
	ds_read_b128 v[204:207], v168 offset:32768
	ds_read_b128 v[208:211], v168 offset:33792
	ds_read_b128 v[212:215], v168 offset:34816
	ds_read_b128 v[216:219], v168 offset:35840
	ds_read_b128 v[220:223], v168 offset:36864
	ds_read_b128 v[224:227], v168 offset:37888
	ds_read_b128 v[228:231], v168 offset:38912
	ds_read_b128 v[232:235], v168 offset:39936
	s_waitcnt vmcnt(8)
	s_waitcnt lgkmcnt(0)
	s_barrier
	s_setprio 1
	s_waitcnt lgkmcnt(0)
	v_mfma_f32_16x16x32_bf16 v[124:127], v[172:175], v[204:207], v[124:127]
	v_mfma_f32_16x16x32_bf16 v[120:123], v[180:183], v[204:207], v[120:123]
	v_mfma_f32_16x16x32_bf16 v[116:119], v[172:175], v[212:215], v[116:119]
	v_mfma_f32_16x16x32_bf16 v[112:115], v[180:183], v[212:215], v[112:115]
	v_mfma_f32_16x16x32_bf16 v[100:103], v[172:175], v[220:223], v[100:103]
	v_mfma_f32_16x16x32_bf16 v[96:99], v[180:183], v[220:223], v[96:99]
	v_mfma_f32_16x16x32_bf16 v[84:87], v[172:175], v[228:231], v[84:87]
	v_mfma_f32_16x16x32_bf16 v[80:83], v[180:183], v[228:231], v[80:83]
	v_mfma_f32_16x16x32_bf16 v[124:127], v[176:179], v[208:211], v[124:127]
	v_mfma_f32_16x16x32_bf16 v[120:123], v[184:187], v[208:211], v[120:123]
	v_mfma_f32_16x16x32_bf16 v[116:119], v[176:179], v[216:219], v[116:119]
	v_mfma_f32_16x16x32_bf16 v[112:115], v[184:187], v[216:219], v[112:115]
	v_mfma_f32_16x16x32_bf16 v[100:103], v[176:179], v[224:227], v[100:103]
	v_mfma_f32_16x16x32_bf16 v[96:99], v[184:187], v[224:227], v[96:99]
	v_mfma_f32_16x16x32_bf16 v[84:87], v[176:179], v[232:235], v[84:87]
	v_mfma_f32_16x16x32_bf16 v[80:83], v[184:187], v[232:235], v[80:83]
	s_setprio 0
	s_setprio 1
	v_mfma_f32_16x16x32_bf16 v[108:111], v[188:191], v[204:207], v[108:111]
	v_mfma_f32_16x16x32_bf16 v[104:107], v[196:199], v[204:207], v[104:107]
	v_mfma_f32_16x16x32_bf16 v[92:95], v[188:191], v[212:215], v[92:95]
	v_mfma_f32_16x16x32_bf16 v[88:91], v[196:199], v[212:215], v[88:91]
	v_mfma_f32_16x16x32_bf16 v[76:79], v[188:191], v[220:223], v[76:79]
	v_mfma_f32_16x16x32_bf16 v[72:75], v[196:199], v[220:223], v[72:75]
	v_mfma_f32_16x16x32_bf16 v[68:71], v[188:191], v[228:231], v[68:71]
	v_mfma_f32_16x16x32_bf16 v[64:67], v[196:199], v[228:231], v[64:67]
	v_mfma_f32_16x16x32_bf16 v[108:111], v[192:195], v[208:211], v[108:111]
	v_mfma_f32_16x16x32_bf16 v[104:107], v[200:203], v[208:211], v[104:107]
	v_mfma_f32_16x16x32_bf16 v[92:95], v[192:195], v[216:219], v[92:95]
	v_mfma_f32_16x16x32_bf16 v[88:91], v[200:203], v[216:219], v[88:91]
	v_mfma_f32_16x16x32_bf16 v[76:79], v[192:195], v[224:227], v[76:79]
	v_mfma_f32_16x16x32_bf16 v[72:75], v[200:203], v[224:227], v[72:75]
	v_mfma_f32_16x16x32_bf16 v[68:71], v[192:195], v[232:235], v[68:71]
	v_mfma_f32_16x16x32_bf16 v[64:67], v[200:203], v[232:235], v[64:67]
	s_setprio 0
	s_barrier
	s_mov_b32 m0, s46
	v_lshl_add_u64 v[236:237], v[240:241], 0, s[12:13]
	global_load_lds_dwordx4 v[236:237], off
	ds_read_b128 v[204:207], v168 offset:49152
	ds_read_b128 v[208:211], v168 offset:50176
	v_lshl_add_u64 v[236:237], v[242:243], 0, s[12:13]
	s_mov_b32 m0, s47
	s_nop 0
	global_load_lds_dwordx4 v[236:237], off
	ds_read_b128 v[212:215], v168 offset:51200
	ds_read_b128 v[216:219], v168 offset:52224
	v_lshl_add_u64 v[236:237], v[238:239], 0, s[14:15]
	v_lshl_add_u64 v[238:239], v[236:237], 0, v[134:135]
	s_mov_b32 m0, s50
	v_lshl_add_u64 v[236:237], v[236:237], 0, v[130:131]
	global_load_lds_dwordx4 v[238:239], off
	ds_read_b128 v[220:223], v168 offset:53248
	ds_read_b128 v[224:227], v168 offset:54272
	s_mov_b32 m0, s52
	s_nop 0
	global_load_lds_dwordx4 v[236:237], off
	ds_read_b128 v[228:231], v168 offset:55296
	ds_read_b128 v[232:235], v168 offset:56320
	v_lshl_add_u64 v[236:237], v[244:245], 0, s[12:13]
	s_mov_b32 m0, s38
	s_nop 0
	global_load_lds_dwordx4 v[236:237], off
	v_lshl_add_u64 v[236:237], v[246:247], 0, s[12:13]
	s_mov_b32 m0, s39
	s_nop 0
	global_load_lds_dwordx4 v[236:237], off
	s_waitcnt vmcnt(8)
	s_waitcnt lgkmcnt(0)
	s_barrier
	s_setprio 1
	s_waitcnt lgkmcnt(0)
	v_mfma_f32_16x16x32_bf16 v[60:63], v[172:175], v[204:207], v[60:63]
	v_mfma_f32_16x16x32_bf16 v[56:59], v[180:183], v[204:207], v[56:59]
	v_mfma_f32_16x16x32_bf16 v[52:55], v[172:175], v[212:215], v[52:55]
	v_mfma_f32_16x16x32_bf16 v[48:51], v[180:183], v[212:215], v[48:51]
	v_mfma_f32_16x16x32_bf16 v[36:39], v[172:175], v[220:223], v[36:39]
	v_mfma_f32_16x16x32_bf16 v[32:35], v[180:183], v[220:223], v[32:35]
	v_mfma_f32_16x16x32_bf16 v[20:23], v[172:175], v[228:231], v[20:23]
	v_mfma_f32_16x16x32_bf16 v[16:19], v[180:183], v[228:231], v[16:19]
	v_mfma_f32_16x16x32_bf16 v[60:63], v[176:179], v[208:211], v[60:63]
	v_mfma_f32_16x16x32_bf16 v[56:59], v[184:187], v[208:211], v[56:59]
	v_mfma_f32_16x16x32_bf16 v[52:55], v[176:179], v[216:219], v[52:55]
	v_mfma_f32_16x16x32_bf16 v[48:51], v[184:187], v[216:219], v[48:51]
	v_mfma_f32_16x16x32_bf16 v[36:39], v[176:179], v[224:227], v[36:39]
	v_mfma_f32_16x16x32_bf16 v[32:35], v[184:187], v[224:227], v[32:35]
	v_mfma_f32_16x16x32_bf16 v[20:23], v[176:179], v[232:235], v[20:23]
	v_mfma_f32_16x16x32_bf16 v[16:19], v[184:187], v[232:235], v[16:19]
	s_setprio 0
	s_setprio 1
	v_mfma_f32_16x16x32_bf16 v[44:47], v[188:191], v[204:207], v[44:47]
	v_mfma_f32_16x16x32_bf16 v[40:43], v[196:199], v[204:207], v[40:43]
	v_mfma_f32_16x16x32_bf16 v[28:31], v[188:191], v[212:215], v[28:31]
	v_mfma_f32_16x16x32_bf16 v[24:27], v[196:199], v[212:215], v[24:27]
	v_mfma_f32_16x16x32_bf16 v[12:15], v[188:191], v[220:223], v[12:15]
	v_mfma_f32_16x16x32_bf16 v[8:11], v[196:199], v[220:223], v[8:11]
	v_mfma_f32_16x16x32_bf16 v[4:7], v[188:191], v[228:231], v[4:7]
	v_mfma_f32_16x16x32_bf16 v[0:3], v[196:199], v[228:231], v[0:3]
	v_mfma_f32_16x16x32_bf16 v[44:47], v[192:195], v[208:211], v[44:47]
	v_mfma_f32_16x16x32_bf16 v[40:43], v[200:203], v[208:211], v[40:43]
	v_mfma_f32_16x16x32_bf16 v[28:31], v[192:195], v[216:219], v[28:31]
	v_mfma_f32_16x16x32_bf16 v[24:27], v[200:203], v[216:219], v[24:27]
	v_mfma_f32_16x16x32_bf16 v[12:15], v[192:195], v[224:227], v[12:15]
	v_mfma_f32_16x16x32_bf16 v[8:11], v[200:203], v[224:227], v[8:11]
	v_mfma_f32_16x16x32_bf16 v[4:7], v[192:195], v[232:235], v[4:7]
	v_mfma_f32_16x16x32_bf16 v[0:3], v[200:203], v[232:235], v[0:3]
	s_setprio 0
	s_barrier
	s_add_i32 s25, s25, 2
	v_lshl_add_u64 v[156:157], v[156:157], 0, s[18:19]
	s_cmp_gt_u32 s25, 29
	v_lshl_add_u64 v[158:159], v[158:159], 0, s[18:19]
	s_cbranch_scc0 .LBB0_187
	s_and_b64 vcc, exec, s[16:17]
	s_cbranch_vccz .LBB0_190
	s_barrier

.LBB0_900:
	v_lshl_add_u64 v[170:171], v[144:145], 0, s[36:37]
	v_add_u32_e32 v186, s41, v168
	v_add_u32_e32 v202, s42, v168
	v_lshl_add_u64 v[174:175], v[170:171], 0, s[22:23]
	s_cmpk_eq_i32 s36, 0xf00
	s_cselect_b64 vcc, -1, 0
	v_lshl_add_u64 v[206:207], v[152:153], 0, s[36:37]
	v_cndmask_b32_e32 v175, v175, v155, vcc
	v_cndmask_b32_e32 v174, v174, v154, vcc
	v_cndmask_b32_e32 v239, v207, v157, vcc
	v_cndmask_b32_e32 v238, v206, v156, vcc
	s_mov_b32 m0, s43
	v_lshl_add_u64 v[240:241], v[158:159], 0, s[36:37]
	global_load_lds_dwordx4 v[240:241], off
	ds_read_b128 v[170:173], v186
	ds_read_b128 v[178:181], v186 offset:1024
	ds_read_b128 v[182:185], v186 offset:2048
	ds_read_b128 v[186:189], v186 offset:3072
	ds_read_b128 v[190:193], v202
	ds_read_b128 v[194:197], v202 offset:1024
	v_lshl_add_u64 v[240:241], v[166:167], 0, s[36:37]
	s_mov_b32 m0, s44
	s_nop 0
	global_load_lds_dwordx4 v[240:241], off
	ds_read_b128 v[198:201], v202 offset:2048
	ds_read_b128 v[202:205], v202 offset:3072
	ds_read_b128 v[206:209], v169
	ds_read_b128 v[210:213], v169 offset:1024
	ds_read_b128 v[214:217], v169 offset:2048
	ds_read_b128 v[218:221], v169 offset:3072
	ds_read_b128 v[222:225], v169 offset:4096
	ds_read_b128 v[226:229], v169 offset:5120
	ds_read_b128 v[230:233], v169 offset:6144
	ds_read_b128 v[234:237], v169 offset:7168
	s_waitcnt vmcnt(8)
	s_waitcnt lgkmcnt(0)
	s_barrier
	s_setprio 1
	s_waitcnt lgkmcnt(0)
	v_mfma_f32_16x16x32_bf16 v[124:127], v[170:173], v[206:209], v[124:127]
	v_mfma_f32_16x16x32_bf16 v[120:123], v[182:185], v[206:209], v[120:123]
	v_mfma_f32_16x16x32_bf16 v[112:115], v[170:173], v[214:217], v[112:115]
	v_mfma_f32_16x16x32_bf16 v[108:111], v[182:185], v[214:217], v[108:111]
	v_mfma_f32_16x16x32_bf16 v[96:99], v[170:173], v[222:225], v[96:99]
	v_mfma_f32_16x16x32_bf16 v[92:95], v[182:185], v[222:225], v[92:95]
	v_mfma_f32_16x16x32_bf16 v[80:83], v[170:173], v[230:233], v[80:83]
	v_mfma_f32_16x16x32_bf16 v[76:79], v[182:185], v[230:233], v[76:79]
	v_mfma_f32_16x16x32_bf16 v[124:127], v[178:181], v[210:213], v[124:127]
	v_mfma_f32_16x16x32_bf16 v[120:123], v[186:189], v[210:213], v[120:123]
	v_mfma_f32_16x16x32_bf16 v[112:115], v[178:181], v[218:221], v[112:115]
	v_mfma_f32_16x16x32_bf16 v[108:111], v[186:189], v[218:221], v[108:111]
	v_mfma_f32_16x16x32_bf16 v[96:99], v[178:181], v[226:229], v[96:99]
	v_mfma_f32_16x16x32_bf16 v[92:95], v[186:189], v[226:229], v[92:95]
	v_mfma_f32_16x16x32_bf16 v[80:83], v[178:181], v[234:237], v[80:83]
	v_mfma_f32_16x16x32_bf16 v[76:79], v[186:189], v[234:237], v[76:79]
	s_setprio 0
	s_setprio 1
	v_mfma_f32_16x16x32_bf16 v[116:119], v[190:193], v[206:209], v[116:119]
	v_mfma_f32_16x16x32_bf16 v[104:107], v[198:201], v[206:209], v[104:107]
	v_mfma_f32_16x16x32_bf16 v[100:103], v[190:193], v[214:217], v[100:103]
	v_mfma_f32_16x16x32_bf16 v[88:91], v[198:201], v[214:217], v[88:91]
	v_mfma_f32_16x16x32_bf16 v[84:87], v[190:193], v[222:225], v[84:87]
	v_mfma_f32_16x16x32_bf16 v[72:75], v[198:201], v[222:225], v[72:75]
	v_mfma_f32_16x16x32_bf16 v[68:71], v[190:193], v[230:233], v[68:71]
	v_mfma_f32_16x16x32_bf16 v[64:67], v[198:201], v[230:233], v[64:67]
	v_mfma_f32_16x16x32_bf16 v[116:119], v[194:197], v[210:213], v[116:119]
	v_mfma_f32_16x16x32_bf16 v[104:107], v[202:205], v[210:213], v[104:107]
	v_mfma_f32_16x16x32_bf16 v[100:103], v[194:197], v[218:221], v[100:103]
	v_mfma_f32_16x16x32_bf16 v[88:91], v[202:205], v[218:221], v[88:91]
	v_mfma_f32_16x16x32_bf16 v[84:87], v[194:197], v[226:229], v[84:87]
	v_mfma_f32_16x16x32_bf16 v[72:75], v[202:205], v[226:229], v[72:75]
	v_mfma_f32_16x16x32_bf16 v[68:71], v[194:197], v[234:237], v[68:71]
	v_mfma_f32_16x16x32_bf16 v[64:67], v[202:205], v[234:237], v[64:67]
	s_setprio 0
	s_barrier
	s_mov_b32 m0, s45
	v_lshl_add_u64 v[240:241], v[238:239], 0, v[132:133]
	global_load_lds_dwordx4 v[240:241], off
	ds_read_b128 v[206:209], v169 offset:16384
	ds_read_b128 v[210:213], v169 offset:17408
	v_lshl_add_u64 v[242:243], v[238:239], 0, v[134:135]
	s_mov_b32 m0, s46
	v_lshl_add_u64 v[244:245], v[238:239], 0, s[14:15]
	global_load_lds_dwordx4 v[242:243], off
	ds_read_b128 v[214:217], v169 offset:18432
	ds_read_b128 v[218:221], v169 offset:19456
	v_lshl_add_u64 v[246:247], v[244:245], 0, v[132:133]
	s_mov_b32 m0, s47
	v_lshl_add_u64 v[244:245], v[244:245], 0, v[134:135]
	global_load_lds_dwordx4 v[246:247], off
	ds_read_b128 v[222:225], v169 offset:20480
	ds_read_b128 v[226:229], v169 offset:21504
	s_mov_b32 m0, s50
	v_lshl_add_u64 v[246:247], v[174:175], 0, v[134:135]
	global_load_lds_dwordx4 v[244:245], off
	ds_read_b128 v[230:233], v169 offset:22528
	ds_read_b128 v[234:237], v169 offset:23552
	v_lshl_add_u64 v[244:245], v[174:175], 0, v[132:133]
	s_mov_b32 m0, s9
	s_nop 0
	global_load_lds_dwordx4 v[244:245], off
	s_mov_b32 m0, s33
	s_nop 0
	global_load_lds_dwordx4 v[246:247], off
	s_waitcnt vmcnt(8)
	s_waitcnt lgkmcnt(0)
	s_barrier
	s_setprio 1
	s_waitcnt lgkmcnt(0)
	v_mfma_f32_16x16x32_bf16 v[60:63], v[170:173], v[206:209], v[60:63]
	v_mfma_f32_16x16x32_bf16 v[56:59], v[182:185], v[206:209], v[56:59]
	v_mfma_f32_16x16x32_bf16 v[48:51], v[170:173], v[214:217], v[48:51]
	v_mfma_f32_16x16x32_bf16 v[44:47], v[182:185], v[214:217], v[44:47]
	v_mfma_f32_16x16x32_bf16 v[32:35], v[170:173], v[222:225], v[32:35]
	v_mfma_f32_16x16x32_bf16 v[28:31], v[182:185], v[222:225], v[28:31]
	v_mfma_f32_16x16x32_bf16 v[16:19], v[170:173], v[230:233], v[16:19]
	v_mfma_f32_16x16x32_bf16 v[8:11], v[182:185], v[230:233], v[8:11]
	v_mfma_f32_16x16x32_bf16 v[60:63], v[178:181], v[210:213], v[60:63]
	v_mfma_f32_16x16x32_bf16 v[56:59], v[186:189], v[210:213], v[56:59]
	v_mfma_f32_16x16x32_bf16 v[48:51], v[178:181], v[218:221], v[48:51]
	v_mfma_f32_16x16x32_bf16 v[44:47], v[186:189], v[218:221], v[44:47]
	v_mfma_f32_16x16x32_bf16 v[32:35], v[178:181], v[226:229], v[32:35]
	v_mfma_f32_16x16x32_bf16 v[28:31], v[186:189], v[226:229], v[28:31]
	v_mfma_f32_16x16x32_bf16 v[16:19], v[178:181], v[234:237], v[16:19]
	v_mfma_f32_16x16x32_bf16 v[8:11], v[186:189], v[234:237], v[8:11]
	s_setprio 0
	s_setprio 1
	v_mfma_f32_16x16x32_bf16 v[52:55], v[190:193], v[206:209], v[52:55]
	v_mfma_f32_16x16x32_bf16 v[40:43], v[198:201], v[206:209], v[40:43]
	v_mfma_f32_16x16x32_bf16 v[36:39], v[190:193], v[214:217], v[36:39]
	v_mfma_f32_16x16x32_bf16 v[24:27], v[198:201], v[214:217], v[24:27]
	v_mfma_f32_16x16x32_bf16 v[20:23], v[190:193], v[222:225], v[20:23]
	v_mfma_f32_16x16x32_bf16 v[12:15], v[198:201], v[222:225], v[12:15]
	v_mfma_f32_16x16x32_bf16 v[4:7], v[190:193], v[230:233], v[4:7]
	v_mfma_f32_16x16x32_bf16 v[0:3], v[198:201], v[230:233], v[0:3]
	v_mfma_f32_16x16x32_bf16 v[52:55], v[194:197], v[210:213], v[52:55]
	v_mfma_f32_16x16x32_bf16 v[40:43], v[202:205], v[210:213], v[40:43]
	v_mfma_f32_16x16x32_bf16 v[36:39], v[194:197], v[218:221], v[36:39]
	v_mfma_f32_16x16x32_bf16 v[24:27], v[202:205], v[218:221], v[24:27]
	v_mfma_f32_16x16x32_bf16 v[20:23], v[194:197], v[226:229], v[20:23]
	v_mfma_f32_16x16x32_bf16 v[12:15], v[202:205], v[226:229], v[12:15]
	v_mfma_f32_16x16x32_bf16 v[4:7], v[194:197], v[234:237], v[4:7]
	v_mfma_f32_16x16x32_bf16 v[0:3], v[202:205], v[234:237], v[0:3]
	s_setprio 0
	s_barrier
	s_add_i32 s0, 0, 0x1c000
	v_add_u32_e32 v186, s51, v168
	v_add_u32_e32 v202, s0, v168
	v_lshl_add_u64 v[174:175], v[174:175], 0, s[14:15]
	s_mov_b32 m0, s35
	v_lshl_add_u64 v[248:249], v[174:175], 0, v[132:133]
	global_load_lds_dwordx4 v[248:249], off
	ds_read_b128 v[170:173], v186
	ds_read_b128 v[178:181], v186 offset:1024
	ds_read_b128 v[182:185], v186 offset:2048
	ds_read_b128 v[186:189], v186 offset:3072
	ds_read_b128 v[190:193], v202
	ds_read_b128 v[194:197], v202 offset:1024
	v_lshl_add_u64 v[174:175], v[174:175], 0, v[134:135]
	s_mov_b32 m0, s38
	s_nop 0
	global_load_lds_dwordx4 v[174:175], off
	ds_read_b128 v[198:201], v202 offset:2048
	ds_read_b128 v[202:205], v202 offset:3072
	ds_read_b128 v[206:209], v169 offset:32768
	ds_read_b128 v[210:213], v169 offset:33792
	ds_read_b128 v[214:217], v169 offset:34816
	ds_read_b128 v[218:221], v169 offset:35840
	ds_read_b128 v[222:225], v169 offset:36864
	ds_read_b128 v[226:229], v169 offset:37888
	ds_read_b128 v[230:233], v169 offset:38912
	ds_read_b128 v[234:237], v169 offset:39936
	s_waitcnt vmcnt(8)
	s_waitcnt lgkmcnt(0)
	s_barrier
	s_setprio 1
	s_waitcnt lgkmcnt(0)
	v_mfma_f32_16x16x32_bf16 v[124:127], v[170:173], v[206:209], v[124:127]
	v_mfma_f32_16x16x32_bf16 v[120:123], v[182:185], v[206:209], v[120:123]
	v_mfma_f32_16x16x32_bf16 v[112:115], v[170:173], v[214:217], v[112:115]
	v_mfma_f32_16x16x32_bf16 v[108:111], v[182:185], v[214:217], v[108:111]
	v_mfma_f32_16x16x32_bf16 v[96:99], v[170:173], v[222:225], v[96:99]
	v_mfma_f32_16x16x32_bf16 v[92:95], v[182:185], v[222:225], v[92:95]
	v_mfma_f32_16x16x32_bf16 v[80:83], v[170:173], v[230:233], v[80:83]
	v_mfma_f32_16x16x32_bf16 v[76:79], v[182:185], v[230:233], v[76:79]
	v_mfma_f32_16x16x32_bf16 v[124:127], v[178:181], v[210:213], v[124:127]
	v_mfma_f32_16x16x32_bf16 v[120:123], v[186:189], v[210:213], v[120:123]
	v_mfma_f32_16x16x32_bf16 v[112:115], v[178:181], v[218:221], v[112:115]
	v_mfma_f32_16x16x32_bf16 v[108:111], v[186:189], v[218:221], v[108:111]
	v_mfma_f32_16x16x32_bf16 v[96:99], v[178:181], v[226:229], v[96:99]
	v_mfma_f32_16x16x32_bf16 v[92:95], v[186:189], v[226:229], v[92:95]
	v_mfma_f32_16x16x32_bf16 v[80:83], v[178:181], v[234:237], v[80:83]
	v_mfma_f32_16x16x32_bf16 v[76:79], v[186:189], v[234:237], v[76:79]
	s_setprio 0
	s_setprio 1
	v_mfma_f32_16x16x32_bf16 v[116:119], v[190:193], v[206:209], v[116:119]
	v_mfma_f32_16x16x32_bf16 v[104:107], v[198:201], v[206:209], v[104:107]
	v_mfma_f32_16x16x32_bf16 v[100:103], v[190:193], v[214:217], v[100:103]
	v_mfma_f32_16x16x32_bf16 v[88:91], v[198:201], v[214:217], v[88:91]
	v_mfma_f32_16x16x32_bf16 v[84:87], v[190:193], v[222:225], v[84:87]
	v_mfma_f32_16x16x32_bf16 v[72:75], v[198:201], v[222:225], v[72:75]
	v_mfma_f32_16x16x32_bf16 v[68:71], v[190:193], v[230:233], v[68:71]
	v_mfma_f32_16x16x32_bf16 v[64:67], v[198:201], v[230:233], v[64:67]
	v_mfma_f32_16x16x32_bf16 v[116:119], v[194:197], v[210:213], v[116:119]
	v_mfma_f32_16x16x32_bf16 v[104:107], v[202:205], v[210:213], v[104:107]
	v_mfma_f32_16x16x32_bf16 v[100:103], v[194:197], v[218:221], v[100:103]
	v_mfma_f32_16x16x32_bf16 v[88:91], v[202:205], v[218:221], v[88:91]
	v_mfma_f32_16x16x32_bf16 v[84:87], v[194:197], v[226:229], v[84:87]
	v_mfma_f32_16x16x32_bf16 v[72:75], v[202:205], v[226:229], v[72:75]
	v_mfma_f32_16x16x32_bf16 v[68:71], v[194:197], v[234:237], v[68:71]
	v_mfma_f32_16x16x32_bf16 v[64:67], v[202:205], v[234:237], v[64:67]
	s_setprio 0
	s_barrier
	s_add_i32 s1, s51, s34
	v_lshl_add_u64 v[174:175], v[240:241], 0, s[18:19]
	s_mov_b32 m0, s1
	ds_read_b128 v[206:209], v169 offset:49152
	global_load_lds_dwordx4 v[174:175], off
	ds_read_b128 v[210:213], v169 offset:50176
	v_lshl_add_u64 v[174:175], v[242:243], 0, s[18:19]
	s_add_i32 m0, s1, 0x2000
	s_add_i32 s0, s0, s34
	global_load_lds_dwordx4 v[174:175], off
	ds_read_b128 v[214:217], v169 offset:51200
	ds_read_b128 v[218:221], v169 offset:52224
	v_lshl_add_u64 v[174:175], v[238:239], 0, s[20:21]
	v_lshl_add_u64 v[238:239], v[174:175], 0, v[132:133]
	s_mov_b32 m0, s0
	v_lshl_add_u64 v[174:175], v[174:175], 0, v[134:135]
	global_load_lds_dwordx4 v[238:239], off
	ds_read_b128 v[222:225], v169 offset:53248
	ds_read_b128 v[226:229], v169 offset:54272
	s_add_i32 m0, s0, 0x2000
	s_nop 0
	global_load_lds_dwordx4 v[174:175], off
	ds_read_b128 v[230:233], v169 offset:55296
	ds_read_b128 v[234:237], v169 offset:56320
	v_lshl_add_u64 v[174:175], v[244:245], 0, s[18:19]
	s_mov_b32 m0, s39
	s_nop 0
	global_load_lds_dwordx4 v[174:175], off
	v_lshl_add_u64 v[174:175], v[246:247], 0, s[18:19]
	s_mov_b32 m0, s40
	s_nop 0
	global_load_lds_dwordx4 v[174:175], off
	s_waitcnt vmcnt(8)
	s_waitcnt lgkmcnt(0)
	s_barrier
	s_setprio 1
	s_waitcnt lgkmcnt(0)
	v_mfma_f32_16x16x32_bf16 v[60:63], v[170:173], v[206:209], v[60:63]
	v_mfma_f32_16x16x32_bf16 v[56:59], v[182:185], v[206:209], v[56:59]
	v_mfma_f32_16x16x32_bf16 v[48:51], v[170:173], v[214:217], v[48:51]
	v_mfma_f32_16x16x32_bf16 v[44:47], v[182:185], v[214:217], v[44:47]
	v_mfma_f32_16x16x32_bf16 v[32:35], v[170:173], v[222:225], v[32:35]
	v_mfma_f32_16x16x32_bf16 v[28:31], v[182:185], v[222:225], v[28:31]
	v_mfma_f32_16x16x32_bf16 v[16:19], v[170:173], v[230:233], v[16:19]
	v_mfma_f32_16x16x32_bf16 v[8:11], v[182:185], v[230:233], v[8:11]
	v_mfma_f32_16x16x32_bf16 v[60:63], v[178:181], v[210:213], v[60:63]
	v_mfma_f32_16x16x32_bf16 v[56:59], v[186:189], v[210:213], v[56:59]
	v_mfma_f32_16x16x32_bf16 v[48:51], v[178:181], v[218:221], v[48:51]
	v_mfma_f32_16x16x32_bf16 v[44:47], v[186:189], v[218:221], v[44:47]
	v_mfma_f32_16x16x32_bf16 v[32:35], v[178:181], v[226:229], v[32:35]
	v_mfma_f32_16x16x32_bf16 v[28:31], v[186:189], v[226:229], v[28:31]
	v_mfma_f32_16x16x32_bf16 v[16:19], v[178:181], v[234:237], v[16:19]
	v_mfma_f32_16x16x32_bf16 v[8:11], v[186:189], v[234:237], v[8:11]
	s_setprio 0
	s_setprio 1
	v_mfma_f32_16x16x32_bf16 v[52:55], v[190:193], v[206:209], v[52:55]
	v_mfma_f32_16x16x32_bf16 v[40:43], v[198:201], v[206:209], v[40:43]
	v_mfma_f32_16x16x32_bf16 v[36:39], v[190:193], v[214:217], v[36:39]
	v_mfma_f32_16x16x32_bf16 v[24:27], v[198:201], v[214:217], v[24:27]
	v_mfma_f32_16x16x32_bf16 v[20:23], v[190:193], v[222:225], v[20:23]
	v_mfma_f32_16x16x32_bf16 v[12:15], v[198:201], v[222:225], v[12:15]
	v_mfma_f32_16x16x32_bf16 v[4:7], v[190:193], v[230:233], v[4:7]
	v_mfma_f32_16x16x32_bf16 v[0:3], v[198:201], v[230:233], v[0:3]
	v_mfma_f32_16x16x32_bf16 v[52:55], v[194:197], v[210:213], v[52:55]
	v_mfma_f32_16x16x32_bf16 v[40:43], v[202:205], v[210:213], v[40:43]
	v_mfma_f32_16x16x32_bf16 v[36:39], v[194:197], v[218:221], v[36:39]
	v_mfma_f32_16x16x32_bf16 v[24:27], v[202:205], v[218:221], v[24:27]
	v_mfma_f32_16x16x32_bf16 v[20:23], v[194:197], v[226:229], v[20:23]
	v_mfma_f32_16x16x32_bf16 v[12:15], v[202:205], v[226:229], v[12:15]
	v_mfma_f32_16x16x32_bf16 v[4:7], v[194:197], v[234:237], v[4:7]
	v_mfma_f32_16x16x32_bf16 v[0:3], v[202:205], v[234:237], v[0:3]
	s_setprio 0
	s_barrier
	s_add_i32 s27, s27, 2
	s_add_u32 s36, s36, 0x100
	s_addc_u32 s37, s37, 0
	s_cmp_gt_u32 s27, 29
	s_cbranch_scc0 .LBB0_900
	s_and_b64 vcc, exec, s[54:55]
	s_cbranch_vccz .LBB0_903
	s_barrier

.LBB0_996:
	v_add_u32_e32 v188, s60, v173
	v_add_u32_e32 v204, s61, v173
	s_mov_b32 s36, 0xfff80080
	s_cmp_eq_u32 s6, s7
	s_mov_b32 s37, -1
	v_lshl_add_u64 v[208:209], v[168:169], 0, s[36:37]
	s_cselect_b64 vcc, -1, 0
	s_add_i32 s7, s7, 2
	v_cndmask_b32_e32 v241, v209, v159, vcc
	v_cndmask_b32_e32 v240, v208, v138, vcc
	v_cndmask_b32_e32 v243, v171, v167, vcc
	v_cndmask_b32_e32 v242, v170, v158, vcc
	v_lshl_add_u64 v[244:245], v[168:169], 0, v[144:145]
	s_add_i32 m0, s19, 0xc000
	ds_read_b128 v[176:179], v188
	global_load_lds_dwordx4 v[244:245], off
	ds_read_b128 v[180:183], v188 offset:1024
	ds_read_b128 v[184:187], v188 offset:2048
	ds_read_b128 v[188:191], v188 offset:3072
	ds_read_b128 v[192:195], v204
	ds_read_b128 v[196:199], v204 offset:1024
	v_lshl_add_u64 v[244:245], v[168:169], 0, v[146:147]
	s_add_i32 m0, s19, 0xe000
	s_nop 0
	global_load_lds_dwordx4 v[244:245], off
	ds_read_b128 v[200:203], v204 offset:2048
	ds_read_b128 v[204:207], v204 offset:3072
	ds_read_b128 v[208:211], v175
	ds_read_b128 v[212:215], v175 offset:1024
	ds_read_b128 v[216:219], v175 offset:2048
	ds_read_b128 v[220:223], v175 offset:3072
	ds_read_b128 v[224:227], v175 offset:4096
	ds_read_b128 v[228:231], v175 offset:5120
	ds_read_b128 v[232:235], v175 offset:6144
	ds_read_b128 v[236:239], v175 offset:7168
	s_waitcnt vmcnt(8)
	s_waitcnt lgkmcnt(0)
	s_barrier
	s_setprio 1
	s_waitcnt lgkmcnt(0)
	v_mfma_f32_16x16x32_bf16 v[124:127], v[176:179], v[208:211], v[124:127]
	v_mfma_f32_16x16x32_bf16 v[116:119], v[184:187], v[208:211], v[116:119]
	v_mfma_f32_16x16x32_bf16 v[108:111], v[176:179], v[216:219], v[108:111]
	v_mfma_f32_16x16x32_bf16 v[100:103], v[184:187], v[216:219], v[100:103]
	v_mfma_f32_16x16x32_bf16 v[92:95], v[176:179], v[224:227], v[92:95]
	v_mfma_f32_16x16x32_bf16 v[84:87], v[184:187], v[224:227], v[84:87]
	v_mfma_f32_16x16x32_bf16 v[76:79], v[176:179], v[232:235], v[76:79]
	v_mfma_f32_16x16x32_bf16 v[68:71], v[184:187], v[232:235], v[68:71]
	v_mfma_f32_16x16x32_bf16 v[124:127], v[180:183], v[212:215], v[124:127]
	v_mfma_f32_16x16x32_bf16 v[116:119], v[188:191], v[212:215], v[116:119]
	v_mfma_f32_16x16x32_bf16 v[108:111], v[180:183], v[220:223], v[108:111]
	v_mfma_f32_16x16x32_bf16 v[100:103], v[188:191], v[220:223], v[100:103]
	v_mfma_f32_16x16x32_bf16 v[92:95], v[180:183], v[228:231], v[92:95]
	v_mfma_f32_16x16x32_bf16 v[84:87], v[188:191], v[228:231], v[84:87]
	v_mfma_f32_16x16x32_bf16 v[76:79], v[180:183], v[236:239], v[76:79]
	v_mfma_f32_16x16x32_bf16 v[68:71], v[188:191], v[236:239], v[68:71]
	s_setprio 0
	s_setprio 1
	v_mfma_f32_16x16x32_bf16 v[120:123], v[192:195], v[208:211], v[120:123]
	v_mfma_f32_16x16x32_bf16 v[112:115], v[200:203], v[208:211], v[112:115]
	v_mfma_f32_16x16x32_bf16 v[104:107], v[192:195], v[216:219], v[104:107]
	v_mfma_f32_16x16x32_bf16 v[96:99], v[200:203], v[216:219], v[96:99]
	v_mfma_f32_16x16x32_bf16 v[88:91], v[192:195], v[224:227], v[88:91]
	v_mfma_f32_16x16x32_bf16 v[80:83], v[200:203], v[224:227], v[80:83]
	v_mfma_f32_16x16x32_bf16 v[72:75], v[192:195], v[232:235], v[72:75]
	v_mfma_f32_16x16x32_bf16 v[64:67], v[200:203], v[232:235], v[64:67]
	v_mfma_f32_16x16x32_bf16 v[120:123], v[196:199], v[212:215], v[120:123]
	v_mfma_f32_16x16x32_bf16 v[112:115], v[204:207], v[212:215], v[112:115]
	v_mfma_f32_16x16x32_bf16 v[104:107], v[196:199], v[220:223], v[104:107]
	v_mfma_f32_16x16x32_bf16 v[96:99], v[204:207], v[220:223], v[96:99]
	v_mfma_f32_16x16x32_bf16 v[88:91], v[196:199], v[228:231], v[88:91]
	v_mfma_f32_16x16x32_bf16 v[80:83], v[204:207], v[228:231], v[80:83]
	v_mfma_f32_16x16x32_bf16 v[72:75], v[196:199], v[236:239], v[72:75]
	v_mfma_f32_16x16x32_bf16 v[64:67], v[204:207], v[236:239], v[64:67]
	s_setprio 0
	s_barrier
	s_add_i32 s0, s60, s34
	v_lshl_add_u64 v[244:245], v[242:243], 0, v[132:133]
	s_mov_b32 m0, s0
	ds_read_b128 v[208:211], v175 offset:16384
	global_load_lds_dwordx4 v[244:245], off
	ds_read_b128 v[212:215], v175 offset:17408
	v_lshl_add_u64 v[246:247], v[242:243], 0, v[136:137]
	s_add_i32 m0, s0, 0x2000
	v_lshl_add_u64 v[248:249], v[242:243], 0, s[8:9]
	s_add_i32 s0, s61, s34
	global_load_lds_dwordx4 v[246:247], off
	ds_read_b128 v[216:219], v175 offset:18432
	ds_read_b128 v[220:223], v175 offset:19456
	v_lshl_add_u64 v[250:251], v[248:249], 0, v[132:133]
	s_mov_b32 m0, s0
	v_lshl_add_u64 v[248:249], v[248:249], 0, v[136:137]
	global_load_lds_dwordx4 v[250:251], off
	ds_read_b128 v[224:227], v175 offset:20480
	ds_read_b128 v[228:231], v175 offset:21504
	s_add_i32 m0, s0, 0x2000
	v_lshl_add_u64 v[250:251], v[240:241], 0, v[134:135]
	global_load_lds_dwordx4 v[248:249], off
	ds_read_b128 v[232:235], v175 offset:22528
	ds_read_b128 v[236:239], v175 offset:23552
	v_lshl_add_u64 v[248:249], v[240:241], 0, v[130:131]
	s_mov_b32 m0, s19
	s_nop 0
	global_load_lds_dwordx4 v[248:249], off
	s_mov_b32 m0, s29
	s_nop 0
	global_load_lds_dwordx4 v[250:251], off
	s_waitcnt vmcnt(8)
	s_waitcnt lgkmcnt(0)
	s_barrier
	s_setprio 1
	s_waitcnt lgkmcnt(0)
	v_mfma_f32_16x16x32_bf16 v[60:63], v[176:179], v[208:211], v[60:63]
	v_mfma_f32_16x16x32_bf16 v[52:55], v[184:187], v[208:211], v[52:55]
	v_mfma_f32_16x16x32_bf16 v[44:47], v[176:179], v[216:219], v[44:47]
	v_mfma_f32_16x16x32_bf16 v[36:39], v[184:187], v[216:219], v[36:39]
	v_mfma_f32_16x16x32_bf16 v[28:31], v[176:179], v[224:227], v[28:31]
	v_mfma_f32_16x16x32_bf16 v[20:23], v[184:187], v[224:227], v[20:23]
	v_mfma_f32_16x16x32_bf16 v[12:15], v[176:179], v[232:235], v[12:15]
	v_mfma_f32_16x16x32_bf16 v[4:7], v[184:187], v[232:235], v[4:7]
	v_mfma_f32_16x16x32_bf16 v[60:63], v[180:183], v[212:215], v[60:63]
	v_mfma_f32_16x16x32_bf16 v[52:55], v[188:191], v[212:215], v[52:55]
	v_mfma_f32_16x16x32_bf16 v[44:47], v[180:183], v[220:223], v[44:47]
	v_mfma_f32_16x16x32_bf16 v[36:39], v[188:191], v[220:223], v[36:39]
	v_mfma_f32_16x16x32_bf16 v[28:31], v[180:183], v[228:231], v[28:31]
	v_mfma_f32_16x16x32_bf16 v[20:23], v[188:191], v[228:231], v[20:23]
	v_mfma_f32_16x16x32_bf16 v[12:15], v[180:183], v[236:239], v[12:15]
	v_mfma_f32_16x16x32_bf16 v[4:7], v[188:191], v[236:239], v[4:7]
	s_setprio 0
	s_setprio 1
	v_mfma_f32_16x16x32_bf16 v[56:59], v[192:195], v[208:211], v[56:59]
	v_mfma_f32_16x16x32_bf16 v[48:51], v[200:203], v[208:211], v[48:51]
	v_mfma_f32_16x16x32_bf16 v[40:43], v[192:195], v[216:219], v[40:43]
	v_mfma_f32_16x16x32_bf16 v[32:35], v[200:203], v[216:219], v[32:35]
	v_mfma_f32_16x16x32_bf16 v[24:27], v[192:195], v[224:227], v[24:27]
	v_mfma_f32_16x16x32_bf16 v[16:19], v[200:203], v[224:227], v[16:19]
	v_mfma_f32_16x16x32_bf16 v[8:11], v[192:195], v[232:235], v[8:11]
	v_mfma_f32_16x16x32_bf16 v[0:3], v[200:203], v[232:235], v[0:3]
	v_mfma_f32_16x16x32_bf16 v[56:59], v[196:199], v[212:215], v[56:59]
	v_mfma_f32_16x16x32_bf16 v[48:51], v[204:207], v[212:215], v[48:51]
	v_mfma_f32_16x16x32_bf16 v[40:43], v[196:199], v[220:223], v[40:43]
	v_mfma_f32_16x16x32_bf16 v[32:35], v[204:207], v[220:223], v[32:35]
	v_mfma_f32_16x16x32_bf16 v[24:27], v[196:199], v[228:231], v[24:27]
	v_mfma_f32_16x16x32_bf16 v[16:19], v[204:207], v[228:231], v[16:19]
	v_mfma_f32_16x16x32_bf16 v[8:11], v[196:199], v[236:239], v[8:11]
	v_mfma_f32_16x16x32_bf16 v[0:3], v[204:207], v[236:239], v[0:3]
	s_setprio 0
	s_barrier
	s_add_i32 s0, 0, 0x18000
	s_add_i32 s1, 0, 0x1c000
	v_add_u32_e32 v188, s0, v173
	v_add_u32_e32 v204, s1, v173
	v_lshl_add_u64 v[240:241], v[240:241], 0, s[8:9]
	s_mov_b32 m0, s31
	v_lshl_add_u64 v[252:253], v[240:241], 0, v[130:131]
	global_load_lds_dwordx4 v[252:253], off
	ds_read_b128 v[176:179], v188
	ds_read_b128 v[180:183], v188 offset:1024
	ds_read_b128 v[184:187], v188 offset:2048
	ds_read_b128 v[188:191], v188 offset:3072
	ds_read_b128 v[192:195], v204
	ds_read_b128 v[196:199], v204 offset:1024
	v_lshl_add_u64 v[240:241], v[240:241], 0, v[134:135]
	s_mov_b32 m0, s44
	s_nop 0
	global_load_lds_dwordx4 v[240:241], off
	ds_read_b128 v[200:203], v204 offset:2048
	ds_read_b128 v[204:207], v204 offset:3072
	ds_read_b128 v[208:211], v175 offset:32768
	ds_read_b128 v[212:215], v175 offset:33792
	ds_read_b128 v[216:219], v175 offset:34816
	ds_read_b128 v[220:223], v175 offset:35840
	ds_read_b128 v[224:227], v175 offset:36864
	ds_read_b128 v[228:231], v175 offset:37888
	ds_read_b128 v[232:235], v175 offset:38912
	ds_read_b128 v[236:239], v175 offset:39936
	s_waitcnt vmcnt(8)
	s_waitcnt lgkmcnt(0)
	s_barrier
	s_setprio 1
	s_waitcnt lgkmcnt(0)
	v_mfma_f32_16x16x32_bf16 v[124:127], v[176:179], v[208:211], v[124:127]
	v_mfma_f32_16x16x32_bf16 v[116:119], v[184:187], v[208:211], v[116:119]
	v_mfma_f32_16x16x32_bf16 v[108:111], v[176:179], v[216:219], v[108:111]
	v_mfma_f32_16x16x32_bf16 v[100:103], v[184:187], v[216:219], v[100:103]
	v_mfma_f32_16x16x32_bf16 v[92:95], v[176:179], v[224:227], v[92:95]
	v_mfma_f32_16x16x32_bf16 v[84:87], v[184:187], v[224:227], v[84:87]
	v_mfma_f32_16x16x32_bf16 v[76:79], v[176:179], v[232:235], v[76:79]
	v_mfma_f32_16x16x32_bf16 v[68:71], v[184:187], v[232:235], v[68:71]
	v_mfma_f32_16x16x32_bf16 v[124:127], v[180:183], v[212:215], v[124:127]
	v_mfma_f32_16x16x32_bf16 v[116:119], v[188:191], v[212:215], v[116:119]
	v_mfma_f32_16x16x32_bf16 v[108:111], v[180:183], v[220:223], v[108:111]
	v_mfma_f32_16x16x32_bf16 v[100:103], v[188:191], v[220:223], v[100:103]
	v_mfma_f32_16x16x32_bf16 v[92:95], v[180:183], v[228:231], v[92:95]
	v_mfma_f32_16x16x32_bf16 v[84:87], v[188:191], v[228:231], v[84:87]
	v_mfma_f32_16x16x32_bf16 v[76:79], v[180:183], v[236:239], v[76:79]
	v_mfma_f32_16x16x32_bf16 v[68:71], v[188:191], v[236:239], v[68:71]
	s_setprio 0
	s_setprio 1
	v_mfma_f32_16x16x32_bf16 v[120:123], v[192:195], v[208:211], v[120:123]
	v_mfma_f32_16x16x32_bf16 v[112:115], v[200:203], v[208:211], v[112:115]
	v_mfma_f32_16x16x32_bf16 v[104:107], v[192:195], v[216:219], v[104:107]
	v_mfma_f32_16x16x32_bf16 v[96:99], v[200:203], v[216:219], v[96:99]
	v_mfma_f32_16x16x32_bf16 v[88:91], v[192:195], v[224:227], v[88:91]
	v_mfma_f32_16x16x32_bf16 v[80:83], v[200:203], v[224:227], v[80:83]
	v_mfma_f32_16x16x32_bf16 v[72:75], v[192:195], v[232:235], v[72:75]
	v_mfma_f32_16x16x32_bf16 v[64:67], v[200:203], v[232:235], v[64:67]
	v_mfma_f32_16x16x32_bf16 v[120:123], v[196:199], v[212:215], v[120:123]
	v_mfma_f32_16x16x32_bf16 v[112:115], v[204:207], v[212:215], v[112:115]
	v_mfma_f32_16x16x32_bf16 v[104:107], v[196:199], v[220:223], v[104:107]
	v_mfma_f32_16x16x32_bf16 v[96:99], v[204:207], v[220:223], v[96:99]
	v_mfma_f32_16x16x32_bf16 v[88:91], v[196:199], v[228:231], v[88:91]
	v_mfma_f32_16x16x32_bf16 v[80:83], v[204:207], v[228:231], v[80:83]
	v_mfma_f32_16x16x32_bf16 v[72:75], v[196:199], v[236:239], v[72:75]
	v_mfma_f32_16x16x32_bf16 v[64:67], v[204:207], v[236:239], v[64:67]
	s_setprio 0
	s_barrier
	s_add_i32 s0, s0, s34
	v_lshl_add_u64 v[240:241], v[244:245], 0, s[14:15]
	s_mov_b32 m0, s0
	ds_read_b128 v[208:211], v175 offset:49152
	global_load_lds_dwordx4 v[240:241], off
	ds_read_b128 v[212:215], v175 offset:50176
	v_lshl_add_u64 v[240:241], v[246:247], 0, s[14:15]
	s_add_i32 m0, s0, 0x2000
	s_add_i32 s0, s1, s34
	global_load_lds_dwordx4 v[240:241], off
	ds_read_b128 v[216:219], v175 offset:51200
	ds_read_b128 v[220:223], v175 offset:52224
	v_lshl_add_u64 v[240:241], v[242:243], 0, s[16:17]
	v_lshl_add_u64 v[242:243], v[240:241], 0, v[132:133]
	s_mov_b32 m0, s0
	v_lshl_add_u64 v[240:241], v[240:241], 0, v[136:137]
	global_load_lds_dwordx4 v[242:243], off
	ds_read_b128 v[224:227], v175 offset:53248
	ds_read_b128 v[228:231], v175 offset:54272
	s_add_i32 m0, s0, 0x2000
	s_nop 0
	global_load_lds_dwordx4 v[240:241], off
	ds_read_b128 v[232:235], v175 offset:55296
	ds_read_b128 v[236:239], v175 offset:56320
	v_lshl_add_u64 v[240:241], v[248:249], 0, s[14:15]
	s_mov_b32 m0, s45
	s_nop 0
	global_load_lds_dwordx4 v[240:241], off
	v_lshl_add_u64 v[240:241], v[250:251], 0, s[14:15]
	s_mov_b32 m0, s46
	s_nop 0
	global_load_lds_dwordx4 v[240:241], off
	s_waitcnt vmcnt(8)
	s_waitcnt lgkmcnt(0)
	s_barrier
	s_setprio 1
	s_waitcnt lgkmcnt(0)
	v_mfma_f32_16x16x32_bf16 v[60:63], v[176:179], v[208:211], v[60:63]
	v_mfma_f32_16x16x32_bf16 v[52:55], v[184:187], v[208:211], v[52:55]
	v_mfma_f32_16x16x32_bf16 v[44:47], v[176:179], v[216:219], v[44:47]
	v_mfma_f32_16x16x32_bf16 v[36:39], v[184:187], v[216:219], v[36:39]
	v_mfma_f32_16x16x32_bf16 v[28:31], v[176:179], v[224:227], v[28:31]
	v_mfma_f32_16x16x32_bf16 v[20:23], v[184:187], v[224:227], v[20:23]
	v_mfma_f32_16x16x32_bf16 v[12:15], v[176:179], v[232:235], v[12:15]
	v_mfma_f32_16x16x32_bf16 v[4:7], v[184:187], v[232:235], v[4:7]
	v_mfma_f32_16x16x32_bf16 v[60:63], v[180:183], v[212:215], v[60:63]
	v_mfma_f32_16x16x32_bf16 v[52:55], v[188:191], v[212:215], v[52:55]
	v_mfma_f32_16x16x32_bf16 v[44:47], v[180:183], v[220:223], v[44:47]
	v_mfma_f32_16x16x32_bf16 v[36:39], v[188:191], v[220:223], v[36:39]
	v_mfma_f32_16x16x32_bf16 v[28:31], v[180:183], v[228:231], v[28:31]
	v_mfma_f32_16x16x32_bf16 v[20:23], v[188:191], v[228:231], v[20:23]
	v_mfma_f32_16x16x32_bf16 v[12:15], v[180:183], v[236:239], v[12:15]
	v_mfma_f32_16x16x32_bf16 v[4:7], v[188:191], v[236:239], v[4:7]
	s_setprio 0
	s_setprio 1
	v_mfma_f32_16x16x32_bf16 v[56:59], v[192:195], v[208:211], v[56:59]
	v_mfma_f32_16x16x32_bf16 v[48:51], v[200:203], v[208:211], v[48:51]
	v_mfma_f32_16x16x32_bf16 v[40:43], v[192:195], v[216:219], v[40:43]
	v_mfma_f32_16x16x32_bf16 v[32:35], v[200:203], v[216:219], v[32:35]
	v_mfma_f32_16x16x32_bf16 v[24:27], v[192:195], v[224:227], v[24:27]
	v_mfma_f32_16x16x32_bf16 v[16:19], v[200:203], v[224:227], v[16:19]
	v_mfma_f32_16x16x32_bf16 v[8:11], v[192:195], v[232:235], v[8:11]
	v_mfma_f32_16x16x32_bf16 v[0:3], v[200:203], v[232:235], v[0:3]
	v_mfma_f32_16x16x32_bf16 v[56:59], v[196:199], v[212:215], v[56:59]
	v_mfma_f32_16x16x32_bf16 v[48:51], v[204:207], v[212:215], v[48:51]
	v_mfma_f32_16x16x32_bf16 v[40:43], v[196:199], v[220:223], v[40:43]
	v_mfma_f32_16x16x32_bf16 v[32:35], v[204:207], v[220:223], v[32:35]
	v_mfma_f32_16x16x32_bf16 v[24:27], v[196:199], v[228:231], v[24:27]
	v_mfma_f32_16x16x32_bf16 v[16:19], v[204:207], v[228:231], v[16:19]
	v_mfma_f32_16x16x32_bf16 v[8:11], v[196:199], v[236:239], v[8:11]
	v_mfma_f32_16x16x32_bf16 v[0:3], v[204:207], v[236:239], v[0:3]
	s_setprio 0
	s_barrier
	v_lshl_add_u64 v[168:169], v[168:169], 0, s[20:21]
	s_cmp_ge_i32 s7, s40
	v_lshl_add_u64 v[170:171], v[170:171], 0, s[20:21]
	s_cbranch_scc0 .LBB0_996
	s_and_b64 vcc, exec, s[54:55]
	s_cbranch_vccz .LBB0_999
	s_barrier

.LBB0_1135:
	v_lshl_add_u64 v[166:167], v[142:143], 0, s[10:11]
	v_add_u32_e32 v159, s39, v157
	v_lshl_add_u64 v[190:191], v[166:167], 0, s[24:25]
	s_cmpk_eq_i32 s10, 0x2b00
	s_cselect_b64 vcc, -1, 0
	v_lshl_add_u64 v[202:203], v[150:151], 0, s[10:11]
	v_cndmask_b32_e32 v191, v191, v145, vcc
	v_cndmask_b32_e32 v190, v190, v144, vcc
	v_cndmask_b32_e32 v235, v203, v147, vcc
	v_cndmask_b32_e32 v234, v202, v146, vcc
	s_mov_b32 m0, s41
	v_lshl_add_u64 v[236:237], v[152:153], 0, s[10:11]
	global_load_lds_dwordx4 v[236:237], off
	ds_read_b128 v[166:169], v159
	ds_read_b128 v[170:173], v159 offset:1024
	ds_read_b128 v[174:177], v159 offset:2048
	ds_read_b128 v[178:181], v159 offset:3072
	v_add_u32_e32 v159, s40, v157
	ds_read_b128 v[182:185], v159
	ds_read_b128 v[186:189], v159 offset:1024
	v_lshl_add_u64 v[236:237], v[154:155], 0, s[10:11]
	s_mov_b32 m0, s42
	s_nop 0
	global_load_lds_dwordx4 v[236:237], off
	ds_read_b128 v[194:197], v159 offset:2048
	ds_read_b128 v[198:201], v159 offset:3072
	ds_read_b128 v[202:205], v158
	ds_read_b128 v[206:209], v158 offset:1024
	ds_read_b128 v[210:213], v158 offset:2048
	ds_read_b128 v[214:217], v158 offset:3072
	ds_read_b128 v[218:221], v158 offset:4096
	ds_read_b128 v[222:225], v158 offset:5120
	ds_read_b128 v[226:229], v158 offset:6144
	ds_read_b128 v[230:233], v158 offset:7168
	s_waitcnt vmcnt(8)
	s_waitcnt lgkmcnt(0)
	s_barrier
	s_setprio 1
	s_waitcnt lgkmcnt(0)
	v_mfma_f32_16x16x32_bf16 v[124:127], v[166:169], v[202:205], v[124:127]
	v_mfma_f32_16x16x32_bf16 v[120:123], v[174:177], v[202:205], v[120:123]
	v_mfma_f32_16x16x32_bf16 v[108:111], v[166:169], v[210:213], v[108:111]
	v_mfma_f32_16x16x32_bf16 v[104:107], v[174:177], v[210:213], v[104:107]
	v_mfma_f32_16x16x32_bf16 v[92:95], v[166:169], v[218:221], v[92:95]
	v_mfma_f32_16x16x32_bf16 v[88:91], v[174:177], v[218:221], v[88:91]
	v_mfma_f32_16x16x32_bf16 v[76:79], v[166:169], v[226:229], v[76:79]
	v_mfma_f32_16x16x32_bf16 v[72:75], v[174:177], v[226:229], v[72:75]
	v_mfma_f32_16x16x32_bf16 v[124:127], v[170:173], v[206:209], v[124:127]
	v_mfma_f32_16x16x32_bf16 v[120:123], v[178:181], v[206:209], v[120:123]
	v_mfma_f32_16x16x32_bf16 v[108:111], v[170:173], v[214:217], v[108:111]
	v_mfma_f32_16x16x32_bf16 v[104:107], v[178:181], v[214:217], v[104:107]
	v_mfma_f32_16x16x32_bf16 v[92:95], v[170:173], v[222:225], v[92:95]
	v_mfma_f32_16x16x32_bf16 v[88:91], v[178:181], v[222:225], v[88:91]
	v_mfma_f32_16x16x32_bf16 v[76:79], v[170:173], v[230:233], v[76:79]
	v_mfma_f32_16x16x32_bf16 v[72:75], v[178:181], v[230:233], v[72:75]
	s_setprio 0
	s_setprio 1
	v_mfma_f32_16x16x32_bf16 v[116:119], v[182:185], v[202:205], v[116:119]
	v_mfma_f32_16x16x32_bf16 v[112:115], v[194:197], v[202:205], v[112:115]
	v_mfma_f32_16x16x32_bf16 v[100:103], v[182:185], v[210:213], v[100:103]
	v_mfma_f32_16x16x32_bf16 v[96:99], v[194:197], v[210:213], v[96:99]
	v_mfma_f32_16x16x32_bf16 v[84:87], v[182:185], v[218:221], v[84:87]
	v_mfma_f32_16x16x32_bf16 v[80:83], v[194:197], v[218:221], v[80:83]
	v_mfma_f32_16x16x32_bf16 v[68:71], v[182:185], v[226:229], v[68:71]
	v_mfma_f32_16x16x32_bf16 v[64:67], v[194:197], v[226:229], v[64:67]
	v_mfma_f32_16x16x32_bf16 v[116:119], v[186:189], v[206:209], v[116:119]
	v_mfma_f32_16x16x32_bf16 v[112:115], v[198:201], v[206:209], v[112:115]
	v_mfma_f32_16x16x32_bf16 v[100:103], v[186:189], v[214:217], v[100:103]
	v_mfma_f32_16x16x32_bf16 v[96:99], v[198:201], v[214:217], v[96:99]
	v_mfma_f32_16x16x32_bf16 v[84:87], v[186:189], v[222:225], v[84:87]
	v_mfma_f32_16x16x32_bf16 v[80:83], v[198:201], v[222:225], v[80:83]
	v_mfma_f32_16x16x32_bf16 v[68:71], v[186:189], v[230:233], v[68:71]
	v_mfma_f32_16x16x32_bf16 v[64:67], v[198:201], v[230:233], v[64:67]
	s_setprio 0
	s_barrier
	s_add_i32 s0, s39, s34
	v_lshl_add_u64 v[236:237], v[234:235], 0, v[130:131]
	s_mov_b32 m0, s0
	ds_read_b128 v[202:205], v158 offset:16384
	global_load_lds_dwordx4 v[236:237], off
	ds_read_b128 v[206:209], v158 offset:17408
	v_lshl_add_u64 v[238:239], v[234:235], 0, v[132:133]
	s_add_i32 m0, s0, 0x2000
	v_lshl_add_u64 v[240:241], v[234:235], 0, s[16:17]
	s_add_i32 s0, s40, s34
	global_load_lds_dwordx4 v[238:239], off
	ds_read_b128 v[210:213], v158 offset:18432
	ds_read_b128 v[214:217], v158 offset:19456
	v_lshl_add_u64 v[242:243], v[240:241], 0, v[130:131]
	s_mov_b32 m0, s0
	v_lshl_add_u64 v[240:241], v[240:241], 0, v[132:133]
	global_load_lds_dwordx4 v[242:243], off
	ds_read_b128 v[218:221], v158 offset:20480
	ds_read_b128 v[222:225], v158 offset:21504
	s_add_i32 m0, s0, 0x2000
	v_lshl_add_u64 v[242:243], v[190:191], 0, v[132:133]
	global_load_lds_dwordx4 v[240:241], off
	ds_read_b128 v[226:229], v158 offset:22528
	ds_read_b128 v[230:233], v158 offset:23552
	v_lshl_add_u64 v[240:241], v[190:191], 0, v[130:131]
	s_mov_b32 m0, s31
	s_nop 0
	global_load_lds_dwordx4 v[240:241], off
	s_mov_b32 m0, s33
	s_nop 0
	global_load_lds_dwordx4 v[242:243], off
	s_waitcnt vmcnt(8)
	s_waitcnt lgkmcnt(0)
	s_barrier
	s_setprio 1
	s_waitcnt lgkmcnt(0)
	v_mfma_f32_16x16x32_bf16 v[60:63], v[166:169], v[202:205], v[60:63]
	v_mfma_f32_16x16x32_bf16 v[56:59], v[174:177], v[202:205], v[56:59]
	v_mfma_f32_16x16x32_bf16 v[44:47], v[166:169], v[210:213], v[44:47]
	v_mfma_f32_16x16x32_bf16 v[40:43], v[174:177], v[210:213], v[40:43]
	v_mfma_f32_16x16x32_bf16 v[28:31], v[166:169], v[218:221], v[28:31]
	v_mfma_f32_16x16x32_bf16 v[24:27], v[174:177], v[218:221], v[24:27]
	v_mfma_f32_16x16x32_bf16 v[12:15], v[166:169], v[226:229], v[12:15]
	v_mfma_f32_16x16x32_bf16 v[8:11], v[174:177], v[226:229], v[8:11]
	v_mfma_f32_16x16x32_bf16 v[60:63], v[170:173], v[206:209], v[60:63]
	v_mfma_f32_16x16x32_bf16 v[56:59], v[178:181], v[206:209], v[56:59]
	v_mfma_f32_16x16x32_bf16 v[44:47], v[170:173], v[214:217], v[44:47]
	v_mfma_f32_16x16x32_bf16 v[40:43], v[178:181], v[214:217], v[40:43]
	v_mfma_f32_16x16x32_bf16 v[28:31], v[170:173], v[222:225], v[28:31]
	v_mfma_f32_16x16x32_bf16 v[24:27], v[178:181], v[222:225], v[24:27]
	v_mfma_f32_16x16x32_bf16 v[12:15], v[170:173], v[230:233], v[12:15]
	v_mfma_f32_16x16x32_bf16 v[8:11], v[178:181], v[230:233], v[8:11]
	s_setprio 0
	s_setprio 1
	v_mfma_f32_16x16x32_bf16 v[52:55], v[182:185], v[202:205], v[52:55]
	v_mfma_f32_16x16x32_bf16 v[48:51], v[194:197], v[202:205], v[48:51]
	v_mfma_f32_16x16x32_bf16 v[36:39], v[182:185], v[210:213], v[36:39]
	v_mfma_f32_16x16x32_bf16 v[32:35], v[194:197], v[210:213], v[32:35]
	v_mfma_f32_16x16x32_bf16 v[20:23], v[182:185], v[218:221], v[20:23]
	v_mfma_f32_16x16x32_bf16 v[16:19], v[194:197], v[218:221], v[16:19]
	v_mfma_f32_16x16x32_bf16 v[4:7], v[182:185], v[226:229], v[4:7]
	v_mfma_f32_16x16x32_bf16 v[0:3], v[194:197], v[226:229], v[0:3]
	v_mfma_f32_16x16x32_bf16 v[52:55], v[186:189], v[206:209], v[52:55]
	v_mfma_f32_16x16x32_bf16 v[48:51], v[198:201], v[206:209], v[48:51]
	v_mfma_f32_16x16x32_bf16 v[36:39], v[186:189], v[214:217], v[36:39]
	v_mfma_f32_16x16x32_bf16 v[32:35], v[198:201], v[214:217], v[32:35]
	v_mfma_f32_16x16x32_bf16 v[20:23], v[186:189], v[222:225], v[20:23]
	v_mfma_f32_16x16x32_bf16 v[16:19], v[198:201], v[222:225], v[16:19]
	v_mfma_f32_16x16x32_bf16 v[4:7], v[186:189], v[230:233], v[4:7]
	v_mfma_f32_16x16x32_bf16 v[0:3], v[198:201], v[230:233], v[0:3]
	s_setprio 0
	s_barrier
	s_add_i32 s0, 0, 0x18000
	v_add_u32_e32 v159, s0, v157
	s_add_i32 s1, 0, 0x1c000
	v_lshl_add_u64 v[190:191], v[190:191], 0, s[16:17]
	s_mov_b32 m0, s35
	v_lshl_add_u64 v[244:245], v[190:191], 0, v[130:131]
	global_load_lds_dwordx4 v[244:245], off
	ds_read_b128 v[166:169], v159
	ds_read_b128 v[170:173], v159 offset:1024
	ds_read_b128 v[174:177], v159 offset:2048
	ds_read_b128 v[178:181], v159 offset:3072
	v_add_u32_e32 v159, s1, v157
	ds_read_b128 v[182:185], v159
	ds_read_b128 v[186:189], v159 offset:1024
	v_lshl_add_u64 v[190:191], v[190:191], 0, v[132:133]
	s_mov_b32 m0, s36
	s_nop 0
	global_load_lds_dwordx4 v[190:191], off
	ds_read_b128 v[194:197], v159 offset:2048
	ds_read_b128 v[198:201], v159 offset:3072
	ds_read_b128 v[202:205], v158 offset:32768
	ds_read_b128 v[206:209], v158 offset:33792
	ds_read_b128 v[210:213], v158 offset:34816
	ds_read_b128 v[214:217], v158 offset:35840
	ds_read_b128 v[218:221], v158 offset:36864
	ds_read_b128 v[222:225], v158 offset:37888
	ds_read_b128 v[226:229], v158 offset:38912
	ds_read_b128 v[230:233], v158 offset:39936
	s_waitcnt vmcnt(8)
	s_waitcnt lgkmcnt(0)
	s_barrier
	s_setprio 1
	s_waitcnt lgkmcnt(0)
	v_mfma_f32_16x16x32_bf16 v[124:127], v[166:169], v[202:205], v[124:127]
	v_mfma_f32_16x16x32_bf16 v[120:123], v[174:177], v[202:205], v[120:123]
	v_mfma_f32_16x16x32_bf16 v[108:111], v[166:169], v[210:213], v[108:111]
	v_mfma_f32_16x16x32_bf16 v[104:107], v[174:177], v[210:213], v[104:107]
	v_mfma_f32_16x16x32_bf16 v[92:95], v[166:169], v[218:221], v[92:95]
	v_mfma_f32_16x16x32_bf16 v[88:91], v[174:177], v[218:221], v[88:91]
	v_mfma_f32_16x16x32_bf16 v[76:79], v[166:169], v[226:229], v[76:79]
	v_mfma_f32_16x16x32_bf16 v[72:75], v[174:177], v[226:229], v[72:75]
	v_mfma_f32_16x16x32_bf16 v[124:127], v[170:173], v[206:209], v[124:127]
	v_mfma_f32_16x16x32_bf16 v[120:123], v[178:181], v[206:209], v[120:123]
	v_mfma_f32_16x16x32_bf16 v[108:111], v[170:173], v[214:217], v[108:111]
	v_mfma_f32_16x16x32_bf16 v[104:107], v[178:181], v[214:217], v[104:107]
	v_mfma_f32_16x16x32_bf16 v[92:95], v[170:173], v[222:225], v[92:95]
	v_mfma_f32_16x16x32_bf16 v[88:91], v[178:181], v[222:225], v[88:91]
	v_mfma_f32_16x16x32_bf16 v[76:79], v[170:173], v[230:233], v[76:79]
	v_mfma_f32_16x16x32_bf16 v[72:75], v[178:181], v[230:233], v[72:75]
	s_setprio 0
	s_setprio 1
	v_mfma_f32_16x16x32_bf16 v[116:119], v[182:185], v[202:205], v[116:119]
	v_mfma_f32_16x16x32_bf16 v[112:115], v[194:197], v[202:205], v[112:115]
	v_mfma_f32_16x16x32_bf16 v[100:103], v[182:185], v[210:213], v[100:103]
	v_mfma_f32_16x16x32_bf16 v[96:99], v[194:197], v[210:213], v[96:99]
	v_mfma_f32_16x16x32_bf16 v[84:87], v[182:185], v[218:221], v[84:87]
	v_mfma_f32_16x16x32_bf16 v[80:83], v[194:197], v[218:221], v[80:83]
	v_mfma_f32_16x16x32_bf16 v[68:71], v[182:185], v[226:229], v[68:71]
	v_mfma_f32_16x16x32_bf16 v[64:67], v[194:197], v[226:229], v[64:67]
	v_mfma_f32_16x16x32_bf16 v[116:119], v[186:189], v[206:209], v[116:119]
	v_mfma_f32_16x16x32_bf16 v[112:115], v[198:201], v[206:209], v[112:115]
	v_mfma_f32_16x16x32_bf16 v[100:103], v[186:189], v[214:217], v[100:103]
	v_mfma_f32_16x16x32_bf16 v[96:99], v[198:201], v[214:217], v[96:99]
	v_mfma_f32_16x16x32_bf16 v[84:87], v[186:189], v[222:225], v[84:87]
	v_mfma_f32_16x16x32_bf16 v[80:83], v[198:201], v[222:225], v[80:83]
	v_mfma_f32_16x16x32_bf16 v[68:71], v[186:189], v[230:233], v[68:71]
	v_mfma_f32_16x16x32_bf16 v[64:67], v[198:201], v[230:233], v[64:67]
	s_setprio 0
	s_barrier
	s_add_i32 s0, s0, s34
	v_lshl_add_u64 v[190:191], v[236:237], 0, s[20:21]
	s_mov_b32 m0, s0
	ds_read_b128 v[202:205], v158 offset:49152
	global_load_lds_dwordx4 v[190:191], off
	ds_read_b128 v[206:209], v158 offset:50176
	v_lshl_add_u64 v[190:191], v[238:239], 0, s[20:21]
	s_add_i32 m0, s0, 0x2000
	s_add_i32 s0, s1, s34
	global_load_lds_dwordx4 v[190:191], off
	ds_read_b128 v[210:213], v158 offset:51200
	ds_read_b128 v[214:217], v158 offset:52224
	v_lshl_add_u64 v[190:191], v[234:235], 0, s[22:23]
	v_lshl_add_u64 v[234:235], v[190:191], 0, v[130:131]
	s_mov_b32 m0, s0
	v_lshl_add_u64 v[190:191], v[190:191], 0, v[132:133]
	global_load_lds_dwordx4 v[234:235], off
	ds_read_b128 v[218:221], v158 offset:53248
	ds_read_b128 v[222:225], v158 offset:54272
	s_add_i32 m0, s0, 0x2000
	s_nop 0
	global_load_lds_dwordx4 v[190:191], off
	ds_read_b128 v[226:229], v158 offset:55296
	ds_read_b128 v[230:233], v158 offset:56320
	v_lshl_add_u64 v[190:191], v[240:241], 0, s[20:21]
	s_mov_b32 m0, s37
	s_nop 0
	global_load_lds_dwordx4 v[190:191], off
	v_lshl_add_u64 v[190:191], v[242:243], 0, s[20:21]
	s_mov_b32 m0, s38
	s_nop 0
	global_load_lds_dwordx4 v[190:191], off
	s_waitcnt vmcnt(8)
	s_waitcnt lgkmcnt(0)
	s_barrier
	s_setprio 1
	s_waitcnt lgkmcnt(0)
	v_mfma_f32_16x16x32_bf16 v[60:63], v[166:169], v[202:205], v[60:63]
	v_mfma_f32_16x16x32_bf16 v[56:59], v[174:177], v[202:205], v[56:59]
	v_mfma_f32_16x16x32_bf16 v[44:47], v[166:169], v[210:213], v[44:47]
	v_mfma_f32_16x16x32_bf16 v[40:43], v[174:177], v[210:213], v[40:43]
	v_mfma_f32_16x16x32_bf16 v[28:31], v[166:169], v[218:221], v[28:31]
	v_mfma_f32_16x16x32_bf16 v[24:27], v[174:177], v[218:221], v[24:27]
	v_mfma_f32_16x16x32_bf16 v[12:15], v[166:169], v[226:229], v[12:15]
	v_mfma_f32_16x16x32_bf16 v[8:11], v[174:177], v[226:229], v[8:11]
	v_mfma_f32_16x16x32_bf16 v[60:63], v[170:173], v[206:209], v[60:63]
	v_mfma_f32_16x16x32_bf16 v[56:59], v[178:181], v[206:209], v[56:59]
	v_mfma_f32_16x16x32_bf16 v[44:47], v[170:173], v[214:217], v[44:47]
	v_mfma_f32_16x16x32_bf16 v[40:43], v[178:181], v[214:217], v[40:43]
	v_mfma_f32_16x16x32_bf16 v[28:31], v[170:173], v[222:225], v[28:31]
	v_mfma_f32_16x16x32_bf16 v[24:27], v[178:181], v[222:225], v[24:27]
	v_mfma_f32_16x16x32_bf16 v[12:15], v[170:173], v[230:233], v[12:15]
	v_mfma_f32_16x16x32_bf16 v[8:11], v[178:181], v[230:233], v[8:11]
	s_setprio 0
	s_setprio 1
	v_mfma_f32_16x16x32_bf16 v[52:55], v[182:185], v[202:205], v[52:55]
	v_mfma_f32_16x16x32_bf16 v[48:51], v[194:197], v[202:205], v[48:51]
	v_mfma_f32_16x16x32_bf16 v[36:39], v[182:185], v[210:213], v[36:39]
	v_mfma_f32_16x16x32_bf16 v[32:35], v[194:197], v[210:213], v[32:35]
	v_mfma_f32_16x16x32_bf16 v[20:23], v[182:185], v[218:221], v[20:23]
	v_mfma_f32_16x16x32_bf16 v[16:19], v[194:197], v[218:221], v[16:19]
	v_mfma_f32_16x16x32_bf16 v[4:7], v[182:185], v[226:229], v[4:7]
	v_mfma_f32_16x16x32_bf16 v[0:3], v[194:197], v[226:229], v[0:3]
	v_mfma_f32_16x16x32_bf16 v[52:55], v[186:189], v[206:209], v[52:55]
	v_mfma_f32_16x16x32_bf16 v[48:51], v[198:201], v[206:209], v[48:51]
	v_mfma_f32_16x16x32_bf16 v[36:39], v[186:189], v[214:217], v[36:39]
	v_mfma_f32_16x16x32_bf16 v[32:35], v[198:201], v[214:217], v[32:35]
	v_mfma_f32_16x16x32_bf16 v[20:23], v[186:189], v[222:225], v[20:23]
	v_mfma_f32_16x16x32_bf16 v[16:19], v[198:201], v[222:225], v[16:19]
	v_mfma_f32_16x16x32_bf16 v[4:7], v[186:189], v[230:233], v[4:7]
	v_mfma_f32_16x16x32_bf16 v[0:3], v[198:201], v[230:233], v[0:3]
	s_setprio 0
	s_barrier
	s_add_i32 s29, s29, 2
	s_add_u32 s10, s10, 0x100
	s_addc_u32 s11, s11, 0
	s_cmpk_gt_u32 s29, 0x55
	s_cbranch_scc0 .LBB0_1135
	s_and_b64 vcc, exec, s[54:55]
	s_cbranch_vccz .LBB0_1138
	s_barrier

.LBB0_1231:
	s_add_i32 s43, s30, 2
	s_add_u32 s0, s28, 0xfff80080
	s_addc_u32 s1, s29, -1
	s_cmp_eq_u32 s40, s30
	s_cselect_b32 s30, s39, s41
	s_cselect_b32 s37, s19, s1
	s_cselect_b32 s36, s21, s0
	s_cselect_b32 s31, s23, s42
	v_lshl_add_u64 v[148:149], s[28:29], 0, v[140:141]
	s_add_i32 m0, s15, 0xc000
	ds_read_b128 v[158:161], v154
	global_load_lds_dwordx4 v[148:149], off
	ds_read_b128 v[162:165], v154 offset:1024
	ds_read_b128 v[166:169], v154 offset:2048
	ds_read_b128 v[170:173], v154 offset:3072
	ds_read_b128 v[174:177], v155
	ds_read_b128 v[178:181], v155 offset:1024
	v_lshl_add_u64 v[148:149], s[28:29], 0, v[142:143]
	s_add_i32 m0, s15, 0xe000
	s_nop 0
	global_load_lds_dwordx4 v[148:149], off
	ds_read_b128 v[182:185], v155 offset:2048
	ds_read_b128 v[186:189], v155 offset:3072
	ds_read_b128 v[190:193], v156
	ds_read_b128 v[194:197], v156 offset:1024
	ds_read_b128 v[198:201], v156 offset:2048
	ds_read_b128 v[202:205], v156 offset:3072
	ds_read_b128 v[206:209], v156 offset:4096
	ds_read_b128 v[210:213], v156 offset:5120
	ds_read_b128 v[214:217], v156 offset:6144
	ds_read_b128 v[218:221], v156 offset:7168
	s_waitcnt vmcnt(8)
	s_waitcnt lgkmcnt(0)
	s_barrier
	s_setprio 1
	s_waitcnt lgkmcnt(0)
	v_mfma_f32_16x16x32_bf16 v[124:127], v[158:161], v[190:193], v[124:127]
	v_mfma_f32_16x16x32_bf16 v[120:123], v[166:169], v[190:193], v[120:123]
	v_mfma_f32_16x16x32_bf16 v[116:119], v[158:161], v[198:201], v[116:119]
	v_mfma_f32_16x16x32_bf16 v[108:111], v[166:169], v[198:201], v[108:111]
	v_mfma_f32_16x16x32_bf16 v[100:103], v[158:161], v[206:209], v[100:103]
	v_mfma_f32_16x16x32_bf16 v[92:95], v[166:169], v[206:209], v[92:95]
	v_mfma_f32_16x16x32_bf16 v[84:87], v[158:161], v[214:217], v[84:87]
	v_mfma_f32_16x16x32_bf16 v[76:79], v[166:169], v[214:217], v[76:79]
	v_mfma_f32_16x16x32_bf16 v[124:127], v[162:165], v[194:197], v[124:127]
	v_mfma_f32_16x16x32_bf16 v[120:123], v[170:173], v[194:197], v[120:123]
	v_mfma_f32_16x16x32_bf16 v[116:119], v[162:165], v[202:205], v[116:119]
	v_mfma_f32_16x16x32_bf16 v[108:111], v[170:173], v[202:205], v[108:111]
	v_mfma_f32_16x16x32_bf16 v[100:103], v[162:165], v[210:213], v[100:103]
	v_mfma_f32_16x16x32_bf16 v[92:95], v[170:173], v[210:213], v[92:95]
	v_mfma_f32_16x16x32_bf16 v[84:87], v[162:165], v[218:221], v[84:87]
	v_mfma_f32_16x16x32_bf16 v[76:79], v[170:173], v[218:221], v[76:79]
	s_setprio 0
	s_setprio 1
	v_mfma_f32_16x16x32_bf16 v[112:115], v[174:177], v[190:193], v[112:115]
	v_mfma_f32_16x16x32_bf16 v[104:107], v[182:185], v[190:193], v[104:107]
	v_mfma_f32_16x16x32_bf16 v[96:99], v[174:177], v[198:201], v[96:99]
	v_mfma_f32_16x16x32_bf16 v[88:91], v[182:185], v[198:201], v[88:91]
	v_mfma_f32_16x16x32_bf16 v[80:83], v[174:177], v[206:209], v[80:83]
	v_mfma_f32_16x16x32_bf16 v[72:75], v[182:185], v[206:209], v[72:75]
	v_mfma_f32_16x16x32_bf16 v[68:71], v[174:177], v[214:217], v[68:71]
	v_mfma_f32_16x16x32_bf16 v[64:67], v[182:185], v[214:217], v[64:67]
	v_mfma_f32_16x16x32_bf16 v[112:115], v[178:181], v[194:197], v[112:115]
	v_mfma_f32_16x16x32_bf16 v[104:107], v[186:189], v[194:197], v[104:107]
	v_mfma_f32_16x16x32_bf16 v[96:99], v[178:181], v[202:205], v[96:99]
	v_mfma_f32_16x16x32_bf16 v[88:91], v[186:189], v[202:205], v[88:91]
	v_mfma_f32_16x16x32_bf16 v[80:83], v[178:181], v[210:213], v[80:83]
	v_mfma_f32_16x16x32_bf16 v[72:75], v[186:189], v[210:213], v[72:75]
	v_mfma_f32_16x16x32_bf16 v[68:71], v[178:181], v[218:221], v[68:71]
	v_mfma_f32_16x16x32_bf16 v[64:67], v[186:189], v[218:221], v[64:67]
	s_setprio 0
	s_barrier
	s_add_i32 s0, s91, s34
	v_lshl_add_u64 v[148:149], s[30:31], 0, v[130:131]
	s_mov_b32 m0, s0
	ds_read_b128 v[190:193], v156 offset:16384
	global_load_lds_dwordx4 v[148:149], off
	ds_read_b128 v[194:197], v156 offset:17408
	s_add_i32 m0, s0, 0x2000
	s_add_u32 s44, s30, 0x80000
	v_lshl_add_u64 v[222:223], s[30:31], 0, v[134:135]
	s_addc_u32 s45, s31, 0
	s_add_i32 s0, s92, s34
	global_load_lds_dwordx4 v[222:223], off
	ds_read_b128 v[198:201], v156 offset:18432
	ds_read_b128 v[202:205], v156 offset:19456
	v_lshl_add_u64 v[224:225], s[44:45], 0, v[130:131]
	s_mov_b32 m0, s0
	v_lshl_add_u64 v[226:227], s[36:37], 0, v[132:133]
	global_load_lds_dwordx4 v[224:225], off
	ds_read_b128 v[206:209], v156 offset:20480
	ds_read_b128 v[210:213], v156 offset:21504
	v_lshl_add_u64 v[224:225], s[44:45], 0, v[134:135]
	s_add_i32 m0, s0, 0x2000
	s_nop 0
	global_load_lds_dwordx4 v[224:225], off
	ds_read_b128 v[214:217], v156 offset:22528
	ds_read_b128 v[218:221], v156 offset:23552
	v_lshl_add_u64 v[224:225], s[36:37], 0, v[128:129]
	s_mov_b32 m0, s15
	s_nop 0
	global_load_lds_dwordx4 v[224:225], off
	s_mov_b32 m0, s17
	s_nop 0
	global_load_lds_dwordx4 v[226:227], off
	s_waitcnt vmcnt(8)
	s_waitcnt lgkmcnt(0)
	s_barrier
	s_setprio 1
	s_waitcnt lgkmcnt(0)
	v_mfma_f32_16x16x32_bf16 v[60:63], v[158:161], v[190:193], v[60:63]
	v_mfma_f32_16x16x32_bf16 v[56:59], v[166:169], v[190:193], v[56:59]
	v_mfma_f32_16x16x32_bf16 v[52:55], v[158:161], v[198:201], v[52:55]
	v_mfma_f32_16x16x32_bf16 v[44:47], v[166:169], v[198:201], v[44:47]
	v_mfma_f32_16x16x32_bf16 v[36:39], v[158:161], v[206:209], v[36:39]
	v_mfma_f32_16x16x32_bf16 v[28:31], v[166:169], v[206:209], v[28:31]
	v_mfma_f32_16x16x32_bf16 v[20:23], v[158:161], v[214:217], v[20:23]
	v_mfma_f32_16x16x32_bf16 v[12:15], v[166:169], v[214:217], v[12:15]
	v_mfma_f32_16x16x32_bf16 v[60:63], v[162:165], v[194:197], v[60:63]
	v_mfma_f32_16x16x32_bf16 v[56:59], v[170:173], v[194:197], v[56:59]
	v_mfma_f32_16x16x32_bf16 v[52:55], v[162:165], v[202:205], v[52:55]
	v_mfma_f32_16x16x32_bf16 v[44:47], v[170:173], v[202:205], v[44:47]
	v_mfma_f32_16x16x32_bf16 v[36:39], v[162:165], v[210:213], v[36:39]
	v_mfma_f32_16x16x32_bf16 v[28:31], v[170:173], v[210:213], v[28:31]
	v_mfma_f32_16x16x32_bf16 v[20:23], v[162:165], v[218:221], v[20:23]
	v_mfma_f32_16x16x32_bf16 v[12:15], v[170:173], v[218:221], v[12:15]
	s_setprio 0
	s_setprio 1
	v_mfma_f32_16x16x32_bf16 v[48:51], v[174:177], v[190:193], v[48:51]
	v_mfma_f32_16x16x32_bf16 v[40:43], v[182:185], v[190:193], v[40:43]
	v_mfma_f32_16x16x32_bf16 v[32:35], v[174:177], v[198:201], v[32:35]
	v_mfma_f32_16x16x32_bf16 v[24:27], v[182:185], v[198:201], v[24:27]
	v_mfma_f32_16x16x32_bf16 v[16:19], v[174:177], v[206:209], v[16:19]
	v_mfma_f32_16x16x32_bf16 v[8:11], v[182:185], v[206:209], v[8:11]
	v_mfma_f32_16x16x32_bf16 v[4:7], v[174:177], v[214:217], v[4:7]
	v_mfma_f32_16x16x32_bf16 v[0:3], v[182:185], v[214:217], v[0:3]
	v_mfma_f32_16x16x32_bf16 v[48:51], v[178:181], v[194:197], v[48:51]
	v_mfma_f32_16x16x32_bf16 v[40:43], v[186:189], v[194:197], v[40:43]
	v_mfma_f32_16x16x32_bf16 v[32:35], v[178:181], v[202:205], v[32:35]
	v_mfma_f32_16x16x32_bf16 v[24:27], v[186:189], v[202:205], v[24:27]
	v_mfma_f32_16x16x32_bf16 v[16:19], v[178:181], v[210:213], v[16:19]
	v_mfma_f32_16x16x32_bf16 v[8:11], v[186:189], v[210:213], v[8:11]
	v_mfma_f32_16x16x32_bf16 v[4:7], v[178:181], v[218:221], v[4:7]
	v_mfma_f32_16x16x32_bf16 v[0:3], v[186:189], v[218:221], v[0:3]
	s_setprio 0
	s_barrier
	s_add_i32 s0, 0, 0x18000
	v_add_u32_e32 v136, s0, v152
	s_add_i32 s1, 0, 0x1c000
	s_add_u32 s36, s36, 0x80000
	s_addc_u32 s37, s37, 0
	s_mov_b32 m0, s82
	v_lshl_add_u64 v[228:229], s[36:37], 0, v[128:129]
	global_load_lds_dwordx4 v[228:229], off
	ds_read_b128 v[158:161], v136
	ds_read_b128 v[162:165], v136 offset:1024
	ds_read_b128 v[166:169], v136 offset:2048
	ds_read_b128 v[170:173], v136 offset:3072
	v_add_u32_e32 v136, s1, v152
	ds_read_b128 v[174:177], v136
	ds_read_b128 v[178:181], v136 offset:1024
	v_lshl_add_u64 v[228:229], s[36:37], 0, v[132:133]
	s_mov_b32 m0, s83
	s_nop 0
	global_load_lds_dwordx4 v[228:229], off
	ds_read_b128 v[182:185], v136 offset:2048
	ds_read_b128 v[186:189], v136 offset:3072
	ds_read_b128 v[190:193], v156 offset:32768
	ds_read_b128 v[194:197], v156 offset:33792
	ds_read_b128 v[198:201], v156 offset:34816
	ds_read_b128 v[202:205], v156 offset:35840
	ds_read_b128 v[206:209], v156 offset:36864
	ds_read_b128 v[210:213], v156 offset:37888
	ds_read_b128 v[214:217], v156 offset:38912
	ds_read_b128 v[218:221], v156 offset:39936
	s_waitcnt vmcnt(8)
	s_waitcnt lgkmcnt(0)
	s_barrier
	s_setprio 1
	s_waitcnt lgkmcnt(0)
	v_mfma_f32_16x16x32_bf16 v[124:127], v[158:161], v[190:193], v[124:127]
	v_mfma_f32_16x16x32_bf16 v[120:123], v[166:169], v[190:193], v[120:123]
	v_mfma_f32_16x16x32_bf16 v[116:119], v[158:161], v[198:201], v[116:119]
	v_mfma_f32_16x16x32_bf16 v[108:111], v[166:169], v[198:201], v[108:111]
	v_mfma_f32_16x16x32_bf16 v[100:103], v[158:161], v[206:209], v[100:103]
	v_mfma_f32_16x16x32_bf16 v[92:95], v[166:169], v[206:209], v[92:95]
	v_mfma_f32_16x16x32_bf16 v[84:87], v[158:161], v[214:217], v[84:87]
	v_mfma_f32_16x16x32_bf16 v[76:79], v[166:169], v[214:217], v[76:79]
	v_mfma_f32_16x16x32_bf16 v[124:127], v[162:165], v[194:197], v[124:127]
	v_mfma_f32_16x16x32_bf16 v[120:123], v[170:173], v[194:197], v[120:123]
	v_mfma_f32_16x16x32_bf16 v[116:119], v[162:165], v[202:205], v[116:119]
	v_mfma_f32_16x16x32_bf16 v[108:111], v[170:173], v[202:205], v[108:111]
	v_mfma_f32_16x16x32_bf16 v[100:103], v[162:165], v[210:213], v[100:103]
	v_mfma_f32_16x16x32_bf16 v[92:95], v[170:173], v[210:213], v[92:95]
	v_mfma_f32_16x16x32_bf16 v[84:87], v[162:165], v[218:221], v[84:87]
	v_mfma_f32_16x16x32_bf16 v[76:79], v[170:173], v[218:221], v[76:79]
	s_setprio 0
	s_setprio 1
	v_mfma_f32_16x16x32_bf16 v[112:115], v[174:177], v[190:193], v[112:115]
	v_mfma_f32_16x16x32_bf16 v[104:107], v[182:185], v[190:193], v[104:107]
	v_mfma_f32_16x16x32_bf16 v[96:99], v[174:177], v[198:201], v[96:99]
	v_mfma_f32_16x16x32_bf16 v[88:91], v[182:185], v[198:201], v[88:91]
	v_mfma_f32_16x16x32_bf16 v[80:83], v[174:177], v[206:209], v[80:83]
	v_mfma_f32_16x16x32_bf16 v[72:75], v[182:185], v[206:209], v[72:75]
	v_mfma_f32_16x16x32_bf16 v[68:71], v[174:177], v[214:217], v[68:71]
	v_mfma_f32_16x16x32_bf16 v[64:67], v[182:185], v[214:217], v[64:67]
	v_mfma_f32_16x16x32_bf16 v[112:115], v[178:181], v[194:197], v[112:115]
	v_mfma_f32_16x16x32_bf16 v[104:107], v[186:189], v[194:197], v[104:107]
	v_mfma_f32_16x16x32_bf16 v[96:99], v[178:181], v[202:205], v[96:99]
	v_mfma_f32_16x16x32_bf16 v[88:91], v[186:189], v[202:205], v[88:91]
	v_mfma_f32_16x16x32_bf16 v[80:83], v[178:181], v[210:213], v[80:83]
	v_mfma_f32_16x16x32_bf16 v[72:75], v[186:189], v[210:213], v[72:75]
	v_mfma_f32_16x16x32_bf16 v[68:71], v[178:181], v[218:221], v[68:71]
	v_mfma_f32_16x16x32_bf16 v[64:67], v[186:189], v[218:221], v[64:67]
	s_setprio 0
	s_barrier
	s_add_i32 s0, s0, s34
	v_lshl_add_u64 v[148:149], v[148:149], 0, s[8:9]
	s_mov_b32 m0, s0
	ds_read_b128 v[190:193], v156 offset:49152
	global_load_lds_dwordx4 v[148:149], off
	ds_read_b128 v[194:197], v156 offset:50176
	s_add_i32 m0, s0, 0x2000
	s_add_u32 s30, s30, 0x80080
	v_lshl_add_u64 v[148:149], v[222:223], 0, s[8:9]
	s_addc_u32 s31, s31, 0
	s_add_i32 s0, s1, s34
	global_load_lds_dwordx4 v[148:149], off
	ds_read_b128 v[198:201], v156 offset:51200
	ds_read_b128 v[202:205], v156 offset:52224
	v_lshl_add_u64 v[148:149], s[30:31], 0, v[130:131]
	s_mov_b32 m0, s0
	s_nop 0
	global_load_lds_dwordx4 v[148:149], off
	ds_read_b128 v[206:209], v156 offset:53248
	ds_read_b128 v[210:213], v156 offset:54272
	v_lshl_add_u64 v[148:149], s[30:31], 0, v[134:135]
	s_add_i32 m0, s0, 0x2000
	s_nop 0
	global_load_lds_dwordx4 v[148:149], off
	ds_read_b128 v[214:217], v156 offset:55296
	ds_read_b128 v[218:221], v156 offset:56320
	v_lshl_add_u64 v[148:149], v[224:225], 0, s[8:9]
	s_mov_b32 m0, s86
	s_nop 0
	global_load_lds_dwordx4 v[148:149], off
	v_lshl_add_u64 v[148:149], v[226:227], 0, s[8:9]
	s_mov_b32 m0, s87
	s_nop 0
	global_load_lds_dwordx4 v[148:149], off
	s_waitcnt vmcnt(8)
	s_waitcnt lgkmcnt(0)
	s_barrier
	s_setprio 1
	s_waitcnt lgkmcnt(0)
	v_mfma_f32_16x16x32_bf16 v[60:63], v[158:161], v[190:193], v[60:63]
	v_mfma_f32_16x16x32_bf16 v[56:59], v[166:169], v[190:193], v[56:59]
	v_mfma_f32_16x16x32_bf16 v[52:55], v[158:161], v[198:201], v[52:55]
	v_mfma_f32_16x16x32_bf16 v[44:47], v[166:169], v[198:201], v[44:47]
	v_mfma_f32_16x16x32_bf16 v[36:39], v[158:161], v[206:209], v[36:39]
	v_mfma_f32_16x16x32_bf16 v[28:31], v[166:169], v[206:209], v[28:31]
	v_mfma_f32_16x16x32_bf16 v[20:23], v[158:161], v[214:217], v[20:23]
	v_mfma_f32_16x16x32_bf16 v[12:15], v[166:169], v[214:217], v[12:15]
	v_mfma_f32_16x16x32_bf16 v[60:63], v[162:165], v[194:197], v[60:63]
	v_mfma_f32_16x16x32_bf16 v[56:59], v[170:173], v[194:197], v[56:59]
	v_mfma_f32_16x16x32_bf16 v[52:55], v[162:165], v[202:205], v[52:55]
	v_mfma_f32_16x16x32_bf16 v[44:47], v[170:173], v[202:205], v[44:47]
	v_mfma_f32_16x16x32_bf16 v[36:39], v[162:165], v[210:213], v[36:39]
	v_mfma_f32_16x16x32_bf16 v[28:31], v[170:173], v[210:213], v[28:31]
	v_mfma_f32_16x16x32_bf16 v[20:23], v[162:165], v[218:221], v[20:23]
	v_mfma_f32_16x16x32_bf16 v[12:15], v[170:173], v[218:221], v[12:15]
	s_setprio 0
	s_setprio 1
	v_mfma_f32_16x16x32_bf16 v[48:51], v[174:177], v[190:193], v[48:51]
	v_mfma_f32_16x16x32_bf16 v[40:43], v[182:185], v[190:193], v[40:43]
	v_mfma_f32_16x16x32_bf16 v[32:35], v[174:177], v[198:201], v[32:35]
	v_mfma_f32_16x16x32_bf16 v[24:27], v[182:185], v[198:201], v[24:27]
	v_mfma_f32_16x16x32_bf16 v[16:19], v[174:177], v[206:209], v[16:19]
	v_mfma_f32_16x16x32_bf16 v[8:11], v[182:185], v[206:209], v[8:11]
	v_mfma_f32_16x16x32_bf16 v[4:7], v[174:177], v[214:217], v[4:7]
	v_mfma_f32_16x16x32_bf16 v[0:3], v[182:185], v[214:217], v[0:3]
	v_mfma_f32_16x16x32_bf16 v[48:51], v[178:181], v[194:197], v[48:51]
	v_mfma_f32_16x16x32_bf16 v[40:43], v[186:189], v[194:197], v[40:43]
	v_mfma_f32_16x16x32_bf16 v[32:35], v[178:181], v[202:205], v[32:35]
	v_mfma_f32_16x16x32_bf16 v[24:27], v[186:189], v[202:205], v[24:27]
	v_mfma_f32_16x16x32_bf16 v[16:19], v[178:181], v[210:213], v[16:19]
	v_mfma_f32_16x16x32_bf16 v[8:11], v[186:189], v[210:213], v[8:11]
	v_mfma_f32_16x16x32_bf16 v[4:7], v[178:181], v[218:221], v[4:7]
	v_mfma_f32_16x16x32_bf16 v[0:3], v[186:189], v[218:221], v[0:3]
	s_setprio 0
	s_barrier
	s_add_u32 s28, s28, 0x100
	s_addc_u32 s29, s29, 0
	s_add_u32 s41, s41, 0x100
	s_addc_u32 s42, s42, 0
	s_cmp_ge_i32 s43, s38
	s_mov_b32 s30, s43
	s_cbranch_scc0 .LBB0_1231
	s_and_b64 vcc, exec, s[54:55]
	s_cbranch_vccz .LBB0_1234
	s_barrier

.LBB0_1994:
	s_add_u32 s0, s38, 0xfff80080
	s_addc_u32 s1, s39, -1
	s_cmp_eq_u32 s69, 28
	s_cselect_b32 s43, s25, s1
	s_cselect_b32 s42, s65, s0
	s_cselect_b32 s41, s27, s68
	s_cselect_b32 s40, s66, s67
	v_lshl_add_u64 v[156:157], s[38:39], 0, v[148:149]
	s_add_i32 m0, s37, 0xc000
	ds_read_b128 v[128:131], v161
	global_load_lds_dwordx4 v[156:157], off
	ds_read_b128 v[132:135], v161 offset:1024
	ds_read_b128 v[136:139], v161 offset:2048
	ds_read_b128 v[140:143], v161 offset:3072
	ds_read_b128 v[164:167], v162
	ds_read_b128 v[168:171], v162 offset:1024
	v_lshl_add_u64 v[156:157], s[38:39], 0, v[150:151]
	s_add_i32 m0, s37, 0xe000
	s_nop 0
	global_load_lds_dwordx4 v[156:157], off
	ds_read_b128 v[172:175], v162 offset:2048
	ds_read_b128 v[176:179], v162 offset:3072
	ds_read_b128 v[180:183], v163
	ds_read_b128 v[184:187], v163 offset:1024
	ds_read_b128 v[188:191], v163 offset:2048
	ds_read_b128 v[192:195], v163 offset:3072
	ds_read_b128 v[196:199], v163 offset:4096
	ds_read_b128 v[200:203], v163 offset:5120
	ds_read_b128 v[204:207], v163 offset:6144
	ds_read_b128 v[208:211], v163 offset:7168
	s_waitcnt vmcnt(8)
	s_waitcnt lgkmcnt(0)
	s_barrier
	s_setprio 1
	s_waitcnt lgkmcnt(0)
	v_mfma_f32_16x16x32_bf16 v[124:127], v[128:131], v[180:183], v[124:127]
	v_mfma_f32_16x16x32_bf16 v[120:123], v[136:139], v[180:183], v[120:123]
	v_mfma_f32_16x16x32_bf16 v[112:115], v[128:131], v[188:191], v[112:115]
	v_mfma_f32_16x16x32_bf16 v[108:111], v[136:139], v[188:191], v[108:111]
	v_mfma_f32_16x16x32_bf16 v[96:99], v[128:131], v[196:199], v[96:99]
	v_mfma_f32_16x16x32_bf16 v[92:95], v[136:139], v[196:199], v[92:95]
	v_mfma_f32_16x16x32_bf16 v[80:83], v[128:131], v[204:207], v[80:83]
	v_mfma_f32_16x16x32_bf16 v[76:79], v[136:139], v[204:207], v[76:79]
	v_mfma_f32_16x16x32_bf16 v[124:127], v[132:135], v[184:187], v[124:127]
	v_mfma_f32_16x16x32_bf16 v[120:123], v[140:143], v[184:187], v[120:123]
	v_mfma_f32_16x16x32_bf16 v[112:115], v[132:135], v[192:195], v[112:115]
	v_mfma_f32_16x16x32_bf16 v[108:111], v[140:143], v[192:195], v[108:111]
	v_mfma_f32_16x16x32_bf16 v[96:99], v[132:135], v[200:203], v[96:99]
	v_mfma_f32_16x16x32_bf16 v[92:95], v[140:143], v[200:203], v[92:95]
	v_mfma_f32_16x16x32_bf16 v[80:83], v[132:135], v[208:211], v[80:83]
	v_mfma_f32_16x16x32_bf16 v[76:79], v[140:143], v[208:211], v[76:79]
	s_setprio 0
	s_setprio 1
	v_mfma_f32_16x16x32_bf16 v[116:119], v[164:167], v[180:183], v[116:119]
	v_mfma_f32_16x16x32_bf16 v[104:107], v[172:175], v[180:183], v[104:107]
	v_mfma_f32_16x16x32_bf16 v[100:103], v[164:167], v[188:191], v[100:103]
	v_mfma_f32_16x16x32_bf16 v[88:91], v[172:175], v[188:191], v[88:91]
	v_mfma_f32_16x16x32_bf16 v[84:87], v[164:167], v[196:199], v[84:87]
	v_mfma_f32_16x16x32_bf16 v[72:75], v[172:175], v[196:199], v[72:75]
	v_mfma_f32_16x16x32_bf16 v[68:71], v[164:167], v[204:207], v[68:71]
	v_mfma_f32_16x16x32_bf16 v[64:67], v[172:175], v[204:207], v[64:67]
	v_mfma_f32_16x16x32_bf16 v[116:119], v[168:171], v[184:187], v[116:119]
	v_mfma_f32_16x16x32_bf16 v[104:107], v[176:179], v[184:187], v[104:107]
	v_mfma_f32_16x16x32_bf16 v[100:103], v[168:171], v[192:195], v[100:103]
	v_mfma_f32_16x16x32_bf16 v[88:91], v[176:179], v[192:195], v[88:91]
	v_mfma_f32_16x16x32_bf16 v[84:87], v[168:171], v[200:203], v[84:87]
	v_mfma_f32_16x16x32_bf16 v[72:75], v[176:179], v[200:203], v[72:75]
	v_mfma_f32_16x16x32_bf16 v[68:71], v[168:171], v[208:211], v[68:71]
	v_mfma_f32_16x16x32_bf16 v[64:67], v[176:179], v[208:211], v[64:67]
	s_setprio 0
	s_barrier
	s_add_i32 s0, s62, s34
	v_lshl_add_u64 v[156:157], s[40:41], 0, v[144:145]
	s_mov_b32 m0, s0
	ds_read_b128 v[180:183], v163 offset:16384
	global_load_lds_dwordx4 v[156:157], off
	ds_read_b128 v[184:187], v163 offset:17408
	s_add_i32 m0, s0, 0x2000
	s_add_u32 s0, s40, 0x80000
	v_lshl_add_u64 v[212:213], s[40:41], 0, v[146:147]
	s_addc_u32 s1, s41, 0
	s_add_i32 s48, s63, s34
	global_load_lds_dwordx4 v[212:213], off
	ds_read_b128 v[188:191], v163 offset:18432
	ds_read_b128 v[192:195], v163 offset:19456
	v_lshl_add_u64 v[214:215], s[0:1], 0, v[144:145]
	s_mov_b32 m0, s48
	v_lshl_add_u64 v[216:217], s[42:43], 0, v[146:147]
	global_load_lds_dwordx4 v[214:215], off
	ds_read_b128 v[196:199], v163 offset:20480
	ds_read_b128 v[200:203], v163 offset:21504
	v_lshl_add_u64 v[214:215], s[0:1], 0, v[146:147]
	s_add_i32 m0, s48, 0x2000
	s_nop 0
	global_load_lds_dwordx4 v[214:215], off
	ds_read_b128 v[204:207], v163 offset:22528
	ds_read_b128 v[208:211], v163 offset:23552
	v_lshl_add_u64 v[214:215], s[42:43], 0, v[144:145]
	s_mov_b32 m0, s37
	s_nop 0
	global_load_lds_dwordx4 v[214:215], off
	s_mov_b32 m0, s47
	s_nop 0
	global_load_lds_dwordx4 v[216:217], off
	s_waitcnt vmcnt(8)
	s_waitcnt lgkmcnt(0)
	s_barrier
	s_setprio 1
	s_waitcnt lgkmcnt(0)
	v_mfma_f32_16x16x32_bf16 v[60:63], v[128:131], v[180:183], v[60:63]
	v_mfma_f32_16x16x32_bf16 v[56:59], v[136:139], v[180:183], v[56:59]
	v_mfma_f32_16x16x32_bf16 v[48:51], v[128:131], v[188:191], v[48:51]
	v_mfma_f32_16x16x32_bf16 v[44:47], v[136:139], v[188:191], v[44:47]
	v_mfma_f32_16x16x32_bf16 v[32:35], v[128:131], v[196:199], v[32:35]
	v_mfma_f32_16x16x32_bf16 v[28:31], v[136:139], v[196:199], v[28:31]
	v_mfma_f32_16x16x32_bf16 v[16:19], v[128:131], v[204:207], v[16:19]
	v_mfma_f32_16x16x32_bf16 v[12:15], v[136:139], v[204:207], v[12:15]
	v_mfma_f32_16x16x32_bf16 v[60:63], v[132:135], v[184:187], v[60:63]
	v_mfma_f32_16x16x32_bf16 v[56:59], v[140:143], v[184:187], v[56:59]
	v_mfma_f32_16x16x32_bf16 v[48:51], v[132:135], v[192:195], v[48:51]
	v_mfma_f32_16x16x32_bf16 v[44:47], v[140:143], v[192:195], v[44:47]
	v_mfma_f32_16x16x32_bf16 v[32:35], v[132:135], v[200:203], v[32:35]
	v_mfma_f32_16x16x32_bf16 v[28:31], v[140:143], v[200:203], v[28:31]
	v_mfma_f32_16x16x32_bf16 v[16:19], v[132:135], v[208:211], v[16:19]
	v_mfma_f32_16x16x32_bf16 v[12:15], v[140:143], v[208:211], v[12:15]
	s_setprio 0
	s_setprio 1
	v_mfma_f32_16x16x32_bf16 v[52:55], v[164:167], v[180:183], v[52:55]
	v_mfma_f32_16x16x32_bf16 v[40:43], v[172:175], v[180:183], v[40:43]
	v_mfma_f32_16x16x32_bf16 v[36:39], v[164:167], v[188:191], v[36:39]
	v_mfma_f32_16x16x32_bf16 v[24:27], v[172:175], v[188:191], v[24:27]
	v_mfma_f32_16x16x32_bf16 v[20:23], v[164:167], v[196:199], v[20:23]
	v_mfma_f32_16x16x32_bf16 v[8:11], v[172:175], v[196:199], v[8:11]
	v_mfma_f32_16x16x32_bf16 v[4:7], v[164:167], v[204:207], v[4:7]
	v_mfma_f32_16x16x32_bf16 v[0:3], v[172:175], v[204:207], v[0:3]
	v_mfma_f32_16x16x32_bf16 v[52:55], v[168:171], v[184:187], v[52:55]
	v_mfma_f32_16x16x32_bf16 v[40:43], v[176:179], v[184:187], v[40:43]
	v_mfma_f32_16x16x32_bf16 v[36:39], v[168:171], v[192:195], v[36:39]
	v_mfma_f32_16x16x32_bf16 v[24:27], v[176:179], v[192:195], v[24:27]
	v_mfma_f32_16x16x32_bf16 v[20:23], v[168:171], v[200:203], v[20:23]
	v_mfma_f32_16x16x32_bf16 v[8:11], v[176:179], v[200:203], v[8:11]
	v_mfma_f32_16x16x32_bf16 v[4:7], v[168:171], v[208:211], v[4:7]
	v_mfma_f32_16x16x32_bf16 v[0:3], v[176:179], v[208:211], v[0:3]
	s_setprio 0
	s_barrier
	s_add_i32 s48, 0, 0x18000
	s_add_i32 s49, 0, 0x1c000
	v_add_u32_e32 v140, s48, v159
	v_add_u32_e32 v176, s49, v159
	s_add_u32 s0, s42, 0x80000
	s_addc_u32 s1, s43, 0
	s_mov_b32 m0, s50
	v_lshl_add_u64 v[218:219], s[0:1], 0, v[144:145]
	global_load_lds_dwordx4 v[218:219], off
	ds_read_b128 v[128:131], v140
	ds_read_b128 v[132:135], v140 offset:1024
	ds_read_b128 v[136:139], v140 offset:2048
	ds_read_b128 v[140:143], v140 offset:3072
	ds_read_b128 v[164:167], v176
	ds_read_b128 v[168:171], v176 offset:1024
	v_lshl_add_u64 v[218:219], s[0:1], 0, v[146:147]
	s_mov_b32 m0, s51
	s_nop 0
	global_load_lds_dwordx4 v[218:219], off
	ds_read_b128 v[172:175], v176 offset:2048
	ds_read_b128 v[176:179], v176 offset:3072
	ds_read_b128 v[180:183], v163 offset:32768
	ds_read_b128 v[184:187], v163 offset:33792
	ds_read_b128 v[188:191], v163 offset:34816
	ds_read_b128 v[192:195], v163 offset:35840
	ds_read_b128 v[196:199], v163 offset:36864
	ds_read_b128 v[200:203], v163 offset:37888
	ds_read_b128 v[204:207], v163 offset:38912
	ds_read_b128 v[208:211], v163 offset:39936
	s_waitcnt vmcnt(8)
	s_waitcnt lgkmcnt(0)
	s_barrier
	s_setprio 1
	s_waitcnt lgkmcnt(0)
	v_mfma_f32_16x16x32_bf16 v[124:127], v[128:131], v[180:183], v[124:127]
	v_mfma_f32_16x16x32_bf16 v[120:123], v[136:139], v[180:183], v[120:123]
	v_mfma_f32_16x16x32_bf16 v[112:115], v[128:131], v[188:191], v[112:115]
	v_mfma_f32_16x16x32_bf16 v[108:111], v[136:139], v[188:191], v[108:111]
	v_mfma_f32_16x16x32_bf16 v[96:99], v[128:131], v[196:199], v[96:99]
	v_mfma_f32_16x16x32_bf16 v[92:95], v[136:139], v[196:199], v[92:95]
	v_mfma_f32_16x16x32_bf16 v[80:83], v[128:131], v[204:207], v[80:83]
	v_mfma_f32_16x16x32_bf16 v[76:79], v[136:139], v[204:207], v[76:79]
	v_mfma_f32_16x16x32_bf16 v[124:127], v[132:135], v[184:187], v[124:127]
	v_mfma_f32_16x16x32_bf16 v[120:123], v[140:143], v[184:187], v[120:123]
	v_mfma_f32_16x16x32_bf16 v[112:115], v[132:135], v[192:195], v[112:115]
	v_mfma_f32_16x16x32_bf16 v[108:111], v[140:143], v[192:195], v[108:111]
	v_mfma_f32_16x16x32_bf16 v[96:99], v[132:135], v[200:203], v[96:99]
	v_mfma_f32_16x16x32_bf16 v[92:95], v[140:143], v[200:203], v[92:95]
	v_mfma_f32_16x16x32_bf16 v[80:83], v[132:135], v[208:211], v[80:83]
	v_mfma_f32_16x16x32_bf16 v[76:79], v[140:143], v[208:211], v[76:79]
	s_setprio 0
	s_setprio 1
	v_mfma_f32_16x16x32_bf16 v[116:119], v[164:167], v[180:183], v[116:119]
	v_mfma_f32_16x16x32_bf16 v[104:107], v[172:175], v[180:183], v[104:107]
	v_mfma_f32_16x16x32_bf16 v[100:103], v[164:167], v[188:191], v[100:103]
	v_mfma_f32_16x16x32_bf16 v[88:91], v[172:175], v[188:191], v[88:91]
	v_mfma_f32_16x16x32_bf16 v[84:87], v[164:167], v[196:199], v[84:87]
	v_mfma_f32_16x16x32_bf16 v[72:75], v[172:175], v[196:199], v[72:75]
	v_mfma_f32_16x16x32_bf16 v[68:71], v[164:167], v[204:207], v[68:71]
	v_mfma_f32_16x16x32_bf16 v[64:67], v[172:175], v[204:207], v[64:67]
	v_mfma_f32_16x16x32_bf16 v[116:119], v[168:171], v[184:187], v[116:119]
	v_mfma_f32_16x16x32_bf16 v[104:107], v[176:179], v[184:187], v[104:107]
	v_mfma_f32_16x16x32_bf16 v[100:103], v[168:171], v[192:195], v[100:103]
	v_mfma_f32_16x16x32_bf16 v[88:91], v[176:179], v[192:195], v[88:91]
	v_mfma_f32_16x16x32_bf16 v[84:87], v[168:171], v[200:203], v[84:87]
	v_mfma_f32_16x16x32_bf16 v[72:75], v[176:179], v[200:203], v[72:75]
	v_mfma_f32_16x16x32_bf16 v[68:71], v[168:171], v[208:211], v[68:71]
	v_mfma_f32_16x16x32_bf16 v[64:67], v[176:179], v[208:211], v[64:67]
	s_setprio 0
	s_barrier
	s_add_i32 s0, s48, s34
	v_lshl_add_u64 v[156:157], v[156:157], 0, s[14:15]
	s_mov_b32 m0, s0
	ds_read_b128 v[180:183], v163 offset:49152
	global_load_lds_dwordx4 v[156:157], off
	ds_read_b128 v[184:187], v163 offset:50176
	s_add_i32 m0, s0, 0x2000
	s_add_u32 s0, s40, 0x80080
	v_lshl_add_u64 v[156:157], v[212:213], 0, s[14:15]
	s_addc_u32 s1, s41, 0
	s_add_i32 s40, s49, s34
	global_load_lds_dwordx4 v[156:157], off
	ds_read_b128 v[188:191], v163 offset:51200
	ds_read_b128 v[192:195], v163 offset:52224
	v_lshl_add_u64 v[156:157], s[0:1], 0, v[144:145]
	s_mov_b32 m0, s40
	s_nop 0
	global_load_lds_dwordx4 v[156:157], off
	ds_read_b128 v[196:199], v163 offset:53248
	ds_read_b128 v[200:203], v163 offset:54272
	v_lshl_add_u64 v[156:157], s[0:1], 0, v[146:147]
	s_add_i32 m0, s40, 0x2000
	s_nop 0
	global_load_lds_dwordx4 v[156:157], off
	ds_read_b128 v[204:207], v163 offset:55296
	ds_read_b128 v[208:211], v163 offset:56320
	v_lshl_add_u64 v[156:157], v[214:215], 0, s[14:15]
	s_mov_b32 m0, s56
	s_nop 0
	global_load_lds_dwordx4 v[156:157], off
	v_lshl_add_u64 v[156:157], v[216:217], 0, s[14:15]
	s_mov_b32 m0, s57
	s_nop 0
	global_load_lds_dwordx4 v[156:157], off
	s_waitcnt vmcnt(8)
	s_waitcnt lgkmcnt(0)
	s_barrier
	s_setprio 1
	s_waitcnt lgkmcnt(0)
	v_mfma_f32_16x16x32_bf16 v[60:63], v[128:131], v[180:183], v[60:63]
	v_mfma_f32_16x16x32_bf16 v[56:59], v[136:139], v[180:183], v[56:59]
	v_mfma_f32_16x16x32_bf16 v[48:51], v[128:131], v[188:191], v[48:51]
	v_mfma_f32_16x16x32_bf16 v[44:47], v[136:139], v[188:191], v[44:47]
	v_mfma_f32_16x16x32_bf16 v[32:35], v[128:131], v[196:199], v[32:35]
	v_mfma_f32_16x16x32_bf16 v[28:31], v[136:139], v[196:199], v[28:31]
	v_mfma_f32_16x16x32_bf16 v[16:19], v[128:131], v[204:207], v[16:19]
	v_mfma_f32_16x16x32_bf16 v[12:15], v[136:139], v[204:207], v[12:15]
	v_mfma_f32_16x16x32_bf16 v[60:63], v[132:135], v[184:187], v[60:63]
	v_mfma_f32_16x16x32_bf16 v[56:59], v[140:143], v[184:187], v[56:59]
	v_mfma_f32_16x16x32_bf16 v[48:51], v[132:135], v[192:195], v[48:51]
	v_mfma_f32_16x16x32_bf16 v[44:47], v[140:143], v[192:195], v[44:47]
	v_mfma_f32_16x16x32_bf16 v[32:35], v[132:135], v[200:203], v[32:35]
	v_mfma_f32_16x16x32_bf16 v[28:31], v[140:143], v[200:203], v[28:31]
	v_mfma_f32_16x16x32_bf16 v[16:19], v[132:135], v[208:211], v[16:19]
	v_mfma_f32_16x16x32_bf16 v[12:15], v[140:143], v[208:211], v[12:15]
	s_setprio 0
	s_setprio 1
	v_mfma_f32_16x16x32_bf16 v[52:55], v[164:167], v[180:183], v[52:55]
	v_mfma_f32_16x16x32_bf16 v[40:43], v[172:175], v[180:183], v[40:43]
	v_mfma_f32_16x16x32_bf16 v[36:39], v[164:167], v[188:191], v[36:39]
	v_mfma_f32_16x16x32_bf16 v[24:27], v[172:175], v[188:191], v[24:27]
	v_mfma_f32_16x16x32_bf16 v[20:23], v[164:167], v[196:199], v[20:23]
	v_mfma_f32_16x16x32_bf16 v[8:11], v[172:175], v[196:199], v[8:11]
	v_mfma_f32_16x16x32_bf16 v[4:7], v[164:167], v[204:207], v[4:7]
	v_mfma_f32_16x16x32_bf16 v[0:3], v[172:175], v[204:207], v[0:3]
	v_mfma_f32_16x16x32_bf16 v[52:55], v[168:171], v[184:187], v[52:55]
	v_mfma_f32_16x16x32_bf16 v[40:43], v[176:179], v[184:187], v[40:43]
	v_mfma_f32_16x16x32_bf16 v[36:39], v[168:171], v[192:195], v[36:39]
	v_mfma_f32_16x16x32_bf16 v[24:27], v[176:179], v[192:195], v[24:27]
	v_mfma_f32_16x16x32_bf16 v[20:23], v[168:171], v[200:203], v[20:23]
	v_mfma_f32_16x16x32_bf16 v[8:11], v[176:179], v[200:203], v[8:11]
	v_mfma_f32_16x16x32_bf16 v[4:7], v[168:171], v[208:211], v[4:7]
	v_mfma_f32_16x16x32_bf16 v[0:3], v[176:179], v[208:211], v[0:3]
	s_setprio 0
	s_barrier
	s_add_i32 s69, s69, 2
	s_add_u32 s38, s38, 0x100
	s_addc_u32 s39, s39, 0
	s_add_u32 s67, s67, 0x100
	s_addc_u32 s68, s68, 0
	s_cmp_gt_u32 s69, 29
	s_cbranch_scc0 .LBB0_1994
	s_and_b64 vcc, exec, s[54:55]
	s_cbranch_vccz .LBB0_1997
	s_barrier

.LBB0_2154:
	s_add_i32 s40, s28, 2
	s_add_u32 s0, s26, 0xfffc0080
	s_addc_u32 s1, s27, -1
	s_cmp_eq_u32 s37, s28
	s_cselect_b32 s28, s17, s38
	s_cselect_b32 s31, s19, s1
	s_cselect_b32 s30, s36, s0
	s_cselect_b32 s29, s15, s39
	v_lshl_add_u64 v[220:221], s[26:27], 0, v[172:173]
	s_add_i32 m0, s25, 0xc000
	ds_read_b128 v[24:27], v191
	global_load_lds_dwordx4 v[220:221], off
	ds_read_b128 v[28:31], v191 offset:1024
	ds_read_b128 v[16:19], v191 offset:2048
	ds_read_b128 v[20:23], v191 offset:3072
	ds_read_b128 v[8:11], v192
	ds_read_b128 v[12:15], v192 offset:1024
	v_lshl_add_u64 v[220:221], s[26:27], 0, v[174:175]
	s_add_i32 m0, s25, 0xe000
	s_nop 0
	global_load_lds_dwordx4 v[220:221], off
	ds_read_b128 v[0:3], v192 offset:2048
	ds_read_b128 v[4:7], v192 offset:3072
	ds_read_b128 v[178:181], v193
	ds_read_b128 v[182:185], v193 offset:1024
	ds_read_b128 v[196:199], v193 offset:2048
	ds_read_b128 v[200:203], v193 offset:3072
	ds_read_b128 v[204:207], v193 offset:4096
	ds_read_b128 v[208:211], v193 offset:5120
	ds_read_b128 v[212:215], v193 offset:6144
	ds_read_b128 v[216:219], v193 offset:7168
	s_waitcnt vmcnt(8)
	s_waitcnt lgkmcnt(0)
	s_barrier
	s_setprio 1
	s_waitcnt lgkmcnt(0)
	v_mfma_scale_f32_16x16x128_f8f6f4 v[156:159], v[24:31], v[178:185], v[156:159], v194, v194 op_sel_hi:[0,0,0]
	v_mfma_scale_f32_16x16x128_f8f6f4 v[152:155], v[16:23], v[178:185], v[152:155], v194, v194 op_sel_hi:[0,0,0]
	v_mfma_scale_f32_16x16x128_f8f6f4 v[140:143], v[24:31], v[196:203], v[140:143], v194, v194 op_sel_hi:[0,0,0]
	v_mfma_scale_f32_16x16x128_f8f6f4 v[136:139], v[16:23], v[196:203], v[136:139], v194, v194 op_sel_hi:[0,0,0]
	v_mfma_scale_f32_16x16x128_f8f6f4 v[124:127], v[24:31], v[204:211], v[124:127], v194, v194 op_sel_hi:[0,0,0]
	v_mfma_scale_f32_16x16x128_f8f6f4 v[120:123], v[16:23], v[204:211], v[120:123], v194, v194 op_sel_hi:[0,0,0]
	v_mfma_scale_f32_16x16x128_f8f6f4 v[108:111], v[24:31], v[212:219], v[108:111], v194, v194 op_sel_hi:[0,0,0]
	v_mfma_scale_f32_16x16x128_f8f6f4 v[104:107], v[16:23], v[212:219], v[104:107], v194, v194 op_sel_hi:[0,0,0]
	s_setprio 0
	s_setprio 1
	v_mfma_scale_f32_16x16x128_f8f6f4 v[148:151], v[8:15], v[178:185], v[148:151], v194, v194 op_sel_hi:[0,0,0]
	v_mfma_scale_f32_16x16x128_f8f6f4 v[144:147], v[0:7], v[178:185], v[144:147], v194, v194 op_sel_hi:[0,0,0]
	v_mfma_scale_f32_16x16x128_f8f6f4 v[132:135], v[8:15], v[196:203], v[132:135], v194, v194 op_sel_hi:[0,0,0]
	v_mfma_scale_f32_16x16x128_f8f6f4 v[128:131], v[0:7], v[196:203], v[128:131], v194, v194 op_sel_hi:[0,0,0]
	v_mfma_scale_f32_16x16x128_f8f6f4 v[116:119], v[8:15], v[204:211], v[116:119], v194, v194 op_sel_hi:[0,0,0]
	v_mfma_scale_f32_16x16x128_f8f6f4 v[112:115], v[0:7], v[204:211], v[112:115], v194, v194 op_sel_hi:[0,0,0]
	v_mfma_scale_f32_16x16x128_f8f6f4 v[100:103], v[8:15], v[212:219], v[100:103], v194, v194 op_sel_hi:[0,0,0]
	v_mfma_scale_f32_16x16x128_f8f6f4 v[96:99], v[0:7], v[212:219], v[96:99], v194, v194 op_sel_hi:[0,0,0]
	s_setprio 0
	s_barrier
	s_add_i32 s0, s81, s34
	v_lshl_add_u64 v[178:179], s[28:29], 0, v[162:163]
	s_mov_b32 m0, s0
	ds_read_b128 v[196:199], v193 offset:16384
	global_load_lds_dwordx4 v[178:179], off
	ds_read_b128 v[200:203], v193 offset:17408
	s_add_i32 m0, s0, 0x2000
	s_add_u32 s0, s28, 0x40000
	v_lshl_add_u64 v[180:181], s[28:29], 0, v[166:167]
	s_addc_u32 s1, s29, 0
	s_add_i32 s41, s82, s34
	global_load_lds_dwordx4 v[180:181], off
	ds_read_b128 v[204:207], v193 offset:18432
	ds_read_b128 v[208:211], v193 offset:19456
	v_lshl_add_u64 v[182:183], s[0:1], 0, v[162:163]
	s_mov_b32 m0, s41
	v_lshl_add_u64 v[184:185], s[30:31], 0, v[164:165]
	global_load_lds_dwordx4 v[182:183], off
	ds_read_b128 v[212:215], v193 offset:20480
	ds_read_b128 v[216:219], v193 offset:21504
	v_lshl_add_u64 v[182:183], s[0:1], 0, v[166:167]
	s_add_i32 m0, s41, 0x2000
	s_nop 0
	global_load_lds_dwordx4 v[182:183], off
	ds_read_b128 v[220:223], v193 offset:22528
	ds_read_b128 v[224:227], v193 offset:23552
	v_lshl_add_u64 v[182:183], s[30:31], 0, v[160:161]
	s_mov_b32 m0, s25
	s_nop 0
	global_load_lds_dwordx4 v[182:183], off
	s_mov_b32 m0, s68
	s_nop 0
	global_load_lds_dwordx4 v[184:185], off
	s_waitcnt vmcnt(8)
	s_waitcnt lgkmcnt(0)
	s_barrier
	s_setprio 1
	s_waitcnt lgkmcnt(0)
	v_mfma_scale_f32_16x16x128_f8f6f4 v[92:95], v[24:31], v[196:203], v[92:95], v194, v194 op_sel_hi:[0,0,0]
	v_mfma_scale_f32_16x16x128_f8f6f4 v[88:91], v[16:23], v[196:203], v[88:91], v194, v194 op_sel_hi:[0,0,0]
	v_mfma_scale_f32_16x16x128_f8f6f4 v[76:79], v[24:31], v[204:211], v[76:79], v194, v194 op_sel_hi:[0,0,0]
	v_mfma_scale_f32_16x16x128_f8f6f4 v[72:75], v[16:23], v[204:211], v[72:75], v194, v194 op_sel_hi:[0,0,0]
	v_mfma_scale_f32_16x16x128_f8f6f4 v[60:63], v[24:31], v[212:219], v[60:63], v194, v194 op_sel_hi:[0,0,0]
	v_mfma_scale_f32_16x16x128_f8f6f4 v[56:59], v[16:23], v[212:219], v[56:59], v194, v194 op_sel_hi:[0,0,0]
	v_mfma_scale_f32_16x16x128_f8f6f4 v[44:47], v[24:31], v[220:227], v[44:47], v194, v194 op_sel_hi:[0,0,0]
	v_mfma_scale_f32_16x16x128_f8f6f4 v[40:43], v[16:23], v[220:227], v[40:43], v194, v194 op_sel_hi:[0,0,0]
	s_setprio 0
	s_setprio 1
	v_mfma_scale_f32_16x16x128_f8f6f4 v[84:87], v[8:15], v[196:203], v[84:87], v194, v194 op_sel_hi:[0,0,0]
	v_mfma_scale_f32_16x16x128_f8f6f4 v[80:83], v[0:7], v[196:203], v[80:83], v194, v194 op_sel_hi:[0,0,0]
	v_mfma_scale_f32_16x16x128_f8f6f4 v[68:71], v[8:15], v[204:211], v[68:71], v194, v194 op_sel_hi:[0,0,0]
	v_mfma_scale_f32_16x16x128_f8f6f4 v[64:67], v[0:7], v[204:211], v[64:67], v194, v194 op_sel_hi:[0,0,0]
	v_mfma_scale_f32_16x16x128_f8f6f4 v[52:55], v[8:15], v[212:219], v[52:55], v194, v194 op_sel_hi:[0,0,0]
	v_mfma_scale_f32_16x16x128_f8f6f4 v[48:51], v[0:7], v[212:219], v[48:51], v194, v194 op_sel_hi:[0,0,0]
	v_mfma_scale_f32_16x16x128_f8f6f4 v[36:39], v[8:15], v[220:227], v[36:39], v194, v194 op_sel_hi:[0,0,0]
	v_mfma_scale_f32_16x16x128_f8f6f4 v[32:35], v[0:7], v[220:227], v[32:35], v194, v194 op_sel_hi:[0,0,0]
	s_setprio 0
	s_barrier
	s_add_i32 s41, 0, 0x18000
	s_add_i32 s42, 0, 0x1c000
	v_add_u32_e32 v12, s41, v188
	v_add_u32_e32 v28, s42, v188
	s_add_u32 s0, s30, 0x40000
	s_addc_u32 s1, s31, 0
	s_mov_b32 m0, s69
	v_lshl_add_u64 v[228:229], s[0:1], 0, v[160:161]
	global_load_lds_dwordx4 v[228:229], off
	ds_read_b128 v[0:3], v12
	ds_read_b128 v[4:7], v12 offset:1024
	ds_read_b128 v[8:11], v12 offset:2048
	ds_read_b128 v[12:15], v12 offset:3072
	ds_read_b128 v[16:19], v28
	ds_read_b128 v[20:23], v28 offset:1024
	v_lshl_add_u64 v[228:229], s[0:1], 0, v[164:165]
	s_mov_b32 m0, s70
	s_nop 0
	global_load_lds_dwordx4 v[228:229], off
	ds_read_b128 v[24:27], v28 offset:2048
	ds_read_b128 v[28:31], v28 offset:3072
	ds_read_b128 v[196:199], v193 offset:32768
	ds_read_b128 v[200:203], v193 offset:33792
	ds_read_b128 v[204:207], v193 offset:34816
	ds_read_b128 v[208:211], v193 offset:35840
	ds_read_b128 v[212:215], v193 offset:36864
	ds_read_b128 v[216:219], v193 offset:37888
	ds_read_b128 v[220:223], v193 offset:38912
	ds_read_b128 v[224:227], v193 offset:39936
	s_waitcnt vmcnt(8)
	s_waitcnt lgkmcnt(0)
	s_barrier
	s_setprio 1
	s_waitcnt lgkmcnt(0)
	v_mfma_scale_f32_16x16x128_f8f6f4 v[156:159], v[0:7], v[196:203], v[156:159], v194, v194 op_sel_hi:[0,0,0]
	v_mfma_scale_f32_16x16x128_f8f6f4 v[152:155], v[8:15], v[196:203], v[152:155], v194, v194 op_sel_hi:[0,0,0]
	v_mfma_scale_f32_16x16x128_f8f6f4 v[140:143], v[0:7], v[204:211], v[140:143], v194, v194 op_sel_hi:[0,0,0]
	v_mfma_scale_f32_16x16x128_f8f6f4 v[136:139], v[8:15], v[204:211], v[136:139], v194, v194 op_sel_hi:[0,0,0]
	v_mfma_scale_f32_16x16x128_f8f6f4 v[124:127], v[0:7], v[212:219], v[124:127], v194, v194 op_sel_hi:[0,0,0]
	v_mfma_scale_f32_16x16x128_f8f6f4 v[120:123], v[8:15], v[212:219], v[120:123], v194, v194 op_sel_hi:[0,0,0]
	v_mfma_scale_f32_16x16x128_f8f6f4 v[108:111], v[0:7], v[220:227], v[108:111], v194, v194 op_sel_hi:[0,0,0]
	v_mfma_scale_f32_16x16x128_f8f6f4 v[104:107], v[8:15], v[220:227], v[104:107], v194, v194 op_sel_hi:[0,0,0]
	s_setprio 0
	s_setprio 1
	v_mfma_scale_f32_16x16x128_f8f6f4 v[148:151], v[16:23], v[196:203], v[148:151], v194, v194 op_sel_hi:[0,0,0]
	v_mfma_scale_f32_16x16x128_f8f6f4 v[144:147], v[24:31], v[196:203], v[144:147], v194, v194 op_sel_hi:[0,0,0]
	v_mfma_scale_f32_16x16x128_f8f6f4 v[132:135], v[16:23], v[204:211], v[132:135], v194, v194 op_sel_hi:[0,0,0]
	v_mfma_scale_f32_16x16x128_f8f6f4 v[128:131], v[24:31], v[204:211], v[128:131], v194, v194 op_sel_hi:[0,0,0]
	v_mfma_scale_f32_16x16x128_f8f6f4 v[116:119], v[16:23], v[212:219], v[116:119], v194, v194 op_sel_hi:[0,0,0]
	v_mfma_scale_f32_16x16x128_f8f6f4 v[112:115], v[24:31], v[212:219], v[112:115], v194, v194 op_sel_hi:[0,0,0]
	v_mfma_scale_f32_16x16x128_f8f6f4 v[100:103], v[16:23], v[220:227], v[100:103], v194, v194 op_sel_hi:[0,0,0]
	v_mfma_scale_f32_16x16x128_f8f6f4 v[96:99], v[24:31], v[220:227], v[96:99], v194, v194 op_sel_hi:[0,0,0]
	s_setprio 0
	s_barrier
	s_add_i32 s0, s41, s34
	v_lshl_add_u64 v[178:179], v[178:179], 0, s[8:9]
	s_mov_b32 m0, s0
	ds_read_b128 v[196:199], v193 offset:49152
	global_load_lds_dwordx4 v[178:179], off
	ds_read_b128 v[200:203], v193 offset:50176
	s_add_i32 m0, s0, 0x2000
	s_add_u32 s0, s28, 0x40080
	v_lshl_add_u64 v[178:179], v[180:181], 0, s[8:9]
	s_addc_u32 s1, s29, 0
	s_add_i32 s28, s42, s34
	global_load_lds_dwordx4 v[178:179], off
	ds_read_b128 v[204:207], v193 offset:51200
	ds_read_b128 v[208:211], v193 offset:52224
	v_lshl_add_u64 v[178:179], s[0:1], 0, v[162:163]
	s_mov_b32 m0, s28
	s_nop 0
	global_load_lds_dwordx4 v[178:179], off
	ds_read_b128 v[212:215], v193 offset:53248
	ds_read_b128 v[216:219], v193 offset:54272
	v_lshl_add_u64 v[178:179], s[0:1], 0, v[166:167]
	s_add_i32 m0, s28, 0x2000
	s_nop 0
	global_load_lds_dwordx4 v[178:179], off
	ds_read_b128 v[220:223], v193 offset:55296
	ds_read_b128 v[224:227], v193 offset:56320
	v_lshl_add_u64 v[178:179], v[182:183], 0, s[8:9]
	s_mov_b32 m0, s73
	s_nop 0
	global_load_lds_dwordx4 v[178:179], off
	v_lshl_add_u64 v[178:179], v[184:185], 0, s[8:9]
	s_mov_b32 m0, s74
	s_nop 0
	global_load_lds_dwordx4 v[178:179], off
	s_waitcnt vmcnt(8)
	s_waitcnt lgkmcnt(0)
	s_barrier
	s_setprio 1
	s_waitcnt lgkmcnt(0)
	v_mfma_scale_f32_16x16x128_f8f6f4 v[92:95], v[0:7], v[196:203], v[92:95], v194, v194 op_sel_hi:[0,0,0]
	v_mfma_scale_f32_16x16x128_f8f6f4 v[88:91], v[8:15], v[196:203], v[88:91], v194, v194 op_sel_hi:[0,0,0]
	v_mfma_scale_f32_16x16x128_f8f6f4 v[76:79], v[0:7], v[204:211], v[76:79], v194, v194 op_sel_hi:[0,0,0]
	v_mfma_scale_f32_16x16x128_f8f6f4 v[72:75], v[8:15], v[204:211], v[72:75], v194, v194 op_sel_hi:[0,0,0]
	v_mfma_scale_f32_16x16x128_f8f6f4 v[60:63], v[0:7], v[212:219], v[60:63], v194, v194 op_sel_hi:[0,0,0]
	v_mfma_scale_f32_16x16x128_f8f6f4 v[56:59], v[8:15], v[212:219], v[56:59], v194, v194 op_sel_hi:[0,0,0]
	v_mfma_scale_f32_16x16x128_f8f6f4 v[44:47], v[0:7], v[220:227], v[44:47], v194, v194 op_sel_hi:[0,0,0]
	v_mfma_scale_f32_16x16x128_f8f6f4 v[40:43], v[8:15], v[220:227], v[40:43], v194, v194 op_sel_hi:[0,0,0]
	s_setprio 0
	s_setprio 1
	v_mfma_scale_f32_16x16x128_f8f6f4 v[84:87], v[16:23], v[196:203], v[84:87], v194, v194 op_sel_hi:[0,0,0]
	v_mfma_scale_f32_16x16x128_f8f6f4 v[80:83], v[24:31], v[196:203], v[80:83], v194, v194 op_sel_hi:[0,0,0]
	v_mfma_scale_f32_16x16x128_f8f6f4 v[68:71], v[16:23], v[204:211], v[68:71], v194, v194 op_sel_hi:[0,0,0]
	v_mfma_scale_f32_16x16x128_f8f6f4 v[64:67], v[24:31], v[204:211], v[64:67], v194, v194 op_sel_hi:[0,0,0]
	v_mfma_scale_f32_16x16x128_f8f6f4 v[52:55], v[16:23], v[212:219], v[52:55], v194, v194 op_sel_hi:[0,0,0]
	v_mfma_scale_f32_16x16x128_f8f6f4 v[48:51], v[24:31], v[212:219], v[48:51], v194, v194 op_sel_hi:[0,0,0]
	v_mfma_scale_f32_16x16x128_f8f6f4 v[36:39], v[16:23], v[220:227], v[36:39], v194, v194 op_sel_hi:[0,0,0]
	v_mfma_scale_f32_16x16x128_f8f6f4 v[32:35], v[24:31], v[220:227], v[32:35], v194, v194 op_sel_hi:[0,0,0]
	s_setprio 0
	s_barrier
	s_add_u32 s26, s26, 0x100
	s_addc_u32 s27, s27, 0
	s_add_u32 s38, s38, 0x100
	s_addc_u32 s39, s39, 0
	s_cmp_ge_i32 s40, s33
	s_mov_b32 s28, s40
	s_cbranch_scc0 .LBB0_2154
	s_nop 15
	s_nop 15
	s_and_b64 vcc, exec, s[54:55]
	s_cbranch_vccz .LBB0_2157
	s_barrier

.LBB0_2316:
	s_add_i32 s36, s28, 2
	s_add_u32 s24, s22, 0x100
	s_addc_u32 s25, s23, 0
	s_cmp_eq_u32 s17, s28
	s_cselect_b32 s28, s20, s24
	s_cselect_b32 s29, s21, s25
	s_cselect_b32 s27, s19, s33
	s_cselect_b32 s26, s18, s31
	v_lshl_add_u64 v[220:221], s[22:23], 0, v[172:173]
	s_add_i32 m0, s63, 0xc000
	ds_read_b128 v[24:27], v191
	global_load_lds_dwordx4 v[220:221], off
	ds_read_b128 v[28:31], v191 offset:1024
	ds_read_b128 v[16:19], v191 offset:2048
	ds_read_b128 v[20:23], v191 offset:3072
	ds_read_b128 v[8:11], v192
	ds_read_b128 v[12:15], v192 offset:1024
	v_lshl_add_u64 v[220:221], s[22:23], 0, v[174:175]
	s_add_i32 m0, s63, 0xe000
	s_nop 0
	global_load_lds_dwordx4 v[220:221], off
	ds_read_b128 v[0:3], v192 offset:2048
	ds_read_b128 v[4:7], v192 offset:3072
	ds_read_b128 v[178:181], v193
	ds_read_b128 v[182:185], v193 offset:1024
	ds_read_b128 v[196:199], v193 offset:2048
	ds_read_b128 v[200:203], v193 offset:3072
	ds_read_b128 v[204:207], v193 offset:4096
	ds_read_b128 v[208:211], v193 offset:5120
	ds_read_b128 v[212:215], v193 offset:6144
	ds_read_b128 v[216:219], v193 offset:7168
	s_waitcnt vmcnt(8)
	s_waitcnt lgkmcnt(0)
	s_barrier
	s_setprio 1
	s_waitcnt lgkmcnt(0)
	v_mfma_scale_f32_16x16x128_f8f6f4 v[156:159], v[24:31], v[178:185], v[156:159], v194, v194 op_sel_hi:[0,0,0]
	v_mfma_scale_f32_16x16x128_f8f6f4 v[152:155], v[16:23], v[178:185], v[152:155], v194, v194 op_sel_hi:[0,0,0]
	v_mfma_scale_f32_16x16x128_f8f6f4 v[140:143], v[24:31], v[196:203], v[140:143], v194, v194 op_sel_hi:[0,0,0]
	v_mfma_scale_f32_16x16x128_f8f6f4 v[136:139], v[16:23], v[196:203], v[136:139], v194, v194 op_sel_hi:[0,0,0]
	v_mfma_scale_f32_16x16x128_f8f6f4 v[124:127], v[24:31], v[204:211], v[124:127], v194, v194 op_sel_hi:[0,0,0]
	v_mfma_scale_f32_16x16x128_f8f6f4 v[120:123], v[16:23], v[204:211], v[120:123], v194, v194 op_sel_hi:[0,0,0]
	v_mfma_scale_f32_16x16x128_f8f6f4 v[108:111], v[24:31], v[212:219], v[108:111], v194, v194 op_sel_hi:[0,0,0]
	v_mfma_scale_f32_16x16x128_f8f6f4 v[104:107], v[16:23], v[212:219], v[104:107], v194, v194 op_sel_hi:[0,0,0]
	s_setprio 0
	s_setprio 1
	v_mfma_scale_f32_16x16x128_f8f6f4 v[148:151], v[8:15], v[178:185], v[148:151], v194, v194 op_sel_hi:[0,0,0]
	v_mfma_scale_f32_16x16x128_f8f6f4 v[144:147], v[0:7], v[178:185], v[144:147], v194, v194 op_sel_hi:[0,0,0]
	v_mfma_scale_f32_16x16x128_f8f6f4 v[132:135], v[8:15], v[196:203], v[132:135], v194, v194 op_sel_hi:[0,0,0]
	v_mfma_scale_f32_16x16x128_f8f6f4 v[128:131], v[0:7], v[196:203], v[128:131], v194, v194 op_sel_hi:[0,0,0]
	v_mfma_scale_f32_16x16x128_f8f6f4 v[116:119], v[8:15], v[204:211], v[116:119], v194, v194 op_sel_hi:[0,0,0]
	v_mfma_scale_f32_16x16x128_f8f6f4 v[112:115], v[0:7], v[204:211], v[112:115], v194, v194 op_sel_hi:[0,0,0]
	v_mfma_scale_f32_16x16x128_f8f6f4 v[100:103], v[8:15], v[212:219], v[100:103], v194, v194 op_sel_hi:[0,0,0]
	v_mfma_scale_f32_16x16x128_f8f6f4 v[96:99], v[0:7], v[212:219], v[96:99], v194, v194 op_sel_hi:[0,0,0]
	s_setprio 0
	s_barrier
	s_add_i32 s0, s77, s34
	v_lshl_add_u64 v[178:179], s[26:27], 0, v[162:163]
	s_mov_b32 m0, s0
	ds_read_b128 v[196:199], v193 offset:16384
	global_load_lds_dwordx4 v[178:179], off
	ds_read_b128 v[200:203], v193 offset:17408
	s_add_i32 m0, s0, 0x2000
	s_add_u32 s0, s26, 0xb0000
	v_lshl_add_u64 v[180:181], s[26:27], 0, v[166:167]
	s_addc_u32 s1, s27, 0
	s_add_i32 s22, s78, s34
	global_load_lds_dwordx4 v[180:181], off
	ds_read_b128 v[204:207], v193 offset:18432
	ds_read_b128 v[208:211], v193 offset:19456
	v_lshl_add_u64 v[182:183], s[0:1], 0, v[162:163]
	s_mov_b32 m0, s22
	v_lshl_add_u64 v[184:185], s[28:29], 0, v[164:165]
	global_load_lds_dwordx4 v[182:183], off
	ds_read_b128 v[212:215], v193 offset:20480
	ds_read_b128 v[216:219], v193 offset:21504
	v_lshl_add_u64 v[182:183], s[0:1], 0, v[166:167]
	s_add_i32 m0, s22, 0x2000
	s_nop 0
	global_load_lds_dwordx4 v[182:183], off
	ds_read_b128 v[220:223], v193 offset:22528
	ds_read_b128 v[224:227], v193 offset:23552
	v_lshl_add_u64 v[182:183], s[28:29], 0, v[160:161]
	s_mov_b32 m0, s63
	s_nop 0
	global_load_lds_dwordx4 v[182:183], off
	s_mov_b32 m0, s64
	s_nop 0
	global_load_lds_dwordx4 v[184:185], off
	s_waitcnt vmcnt(8)
	s_waitcnt lgkmcnt(0)
	s_barrier
	s_setprio 1
	s_waitcnt lgkmcnt(0)
	v_mfma_scale_f32_16x16x128_f8f6f4 v[92:95], v[24:31], v[196:203], v[92:95], v194, v194 op_sel_hi:[0,0,0]
	v_mfma_scale_f32_16x16x128_f8f6f4 v[88:91], v[16:23], v[196:203], v[88:91], v194, v194 op_sel_hi:[0,0,0]
	v_mfma_scale_f32_16x16x128_f8f6f4 v[76:79], v[24:31], v[204:211], v[76:79], v194, v194 op_sel_hi:[0,0,0]
	v_mfma_scale_f32_16x16x128_f8f6f4 v[72:75], v[16:23], v[204:211], v[72:75], v194, v194 op_sel_hi:[0,0,0]
	v_mfma_scale_f32_16x16x128_f8f6f4 v[60:63], v[24:31], v[212:219], v[60:63], v194, v194 op_sel_hi:[0,0,0]
	v_mfma_scale_f32_16x16x128_f8f6f4 v[56:59], v[16:23], v[212:219], v[56:59], v194, v194 op_sel_hi:[0,0,0]
	v_mfma_scale_f32_16x16x128_f8f6f4 v[44:47], v[24:31], v[220:227], v[44:47], v194, v194 op_sel_hi:[0,0,0]
	v_mfma_scale_f32_16x16x128_f8f6f4 v[40:43], v[16:23], v[220:227], v[40:43], v194, v194 op_sel_hi:[0,0,0]
	s_setprio 0
	s_setprio 1
	v_mfma_scale_f32_16x16x128_f8f6f4 v[84:87], v[8:15], v[196:203], v[84:87], v194, v194 op_sel_hi:[0,0,0]
	v_mfma_scale_f32_16x16x128_f8f6f4 v[80:83], v[0:7], v[196:203], v[80:83], v194, v194 op_sel_hi:[0,0,0]
	v_mfma_scale_f32_16x16x128_f8f6f4 v[68:71], v[8:15], v[204:211], v[68:71], v194, v194 op_sel_hi:[0,0,0]
	v_mfma_scale_f32_16x16x128_f8f6f4 v[64:67], v[0:7], v[204:211], v[64:67], v194, v194 op_sel_hi:[0,0,0]
	v_mfma_scale_f32_16x16x128_f8f6f4 v[52:55], v[8:15], v[212:219], v[52:55], v194, v194 op_sel_hi:[0,0,0]
	v_mfma_scale_f32_16x16x128_f8f6f4 v[48:51], v[0:7], v[212:219], v[48:51], v194, v194 op_sel_hi:[0,0,0]
	v_mfma_scale_f32_16x16x128_f8f6f4 v[36:39], v[8:15], v[220:227], v[36:39], v194, v194 op_sel_hi:[0,0,0]
	v_mfma_scale_f32_16x16x128_f8f6f4 v[32:35], v[0:7], v[220:227], v[32:35], v194, v194 op_sel_hi:[0,0,0]
	s_setprio 0
	s_barrier
	s_add_i32 s22, 0, 0x18000
	s_add_i32 s23, 0, 0x1c000
	v_add_u32_e32 v12, s22, v188
	v_add_u32_e32 v28, s23, v188
	s_add_u32 s0, s28, 0xb0000
	s_addc_u32 s1, s29, 0
	s_mov_b32 m0, s65
	v_lshl_add_u64 v[228:229], s[0:1], 0, v[160:161]
	global_load_lds_dwordx4 v[228:229], off
	ds_read_b128 v[0:3], v12
	ds_read_b128 v[4:7], v12 offset:1024
	ds_read_b128 v[8:11], v12 offset:2048
	ds_read_b128 v[12:15], v12 offset:3072
	ds_read_b128 v[16:19], v28
	ds_read_b128 v[20:23], v28 offset:1024
	v_lshl_add_u64 v[228:229], s[0:1], 0, v[164:165]
	s_mov_b32 m0, s66
	s_nop 0
	global_load_lds_dwordx4 v[228:229], off
	ds_read_b128 v[24:27], v28 offset:2048
	ds_read_b128 v[28:31], v28 offset:3072
	ds_read_b128 v[196:199], v193 offset:32768
	ds_read_b128 v[200:203], v193 offset:33792
	ds_read_b128 v[204:207], v193 offset:34816
	ds_read_b128 v[208:211], v193 offset:35840
	ds_read_b128 v[212:215], v193 offset:36864
	ds_read_b128 v[216:219], v193 offset:37888
	ds_read_b128 v[220:223], v193 offset:38912
	ds_read_b128 v[224:227], v193 offset:39936
	s_waitcnt vmcnt(8)
	s_waitcnt lgkmcnt(0)
	s_barrier
	s_setprio 1
	s_waitcnt lgkmcnt(0)
	v_mfma_scale_f32_16x16x128_f8f6f4 v[156:159], v[0:7], v[196:203], v[156:159], v194, v194 op_sel_hi:[0,0,0]
	v_mfma_scale_f32_16x16x128_f8f6f4 v[152:155], v[8:15], v[196:203], v[152:155], v194, v194 op_sel_hi:[0,0,0]
	v_mfma_scale_f32_16x16x128_f8f6f4 v[140:143], v[0:7], v[204:211], v[140:143], v194, v194 op_sel_hi:[0,0,0]
	v_mfma_scale_f32_16x16x128_f8f6f4 v[136:139], v[8:15], v[204:211], v[136:139], v194, v194 op_sel_hi:[0,0,0]
	v_mfma_scale_f32_16x16x128_f8f6f4 v[124:127], v[0:7], v[212:219], v[124:127], v194, v194 op_sel_hi:[0,0,0]
	v_mfma_scale_f32_16x16x128_f8f6f4 v[120:123], v[8:15], v[212:219], v[120:123], v194, v194 op_sel_hi:[0,0,0]
	v_mfma_scale_f32_16x16x128_f8f6f4 v[108:111], v[0:7], v[220:227], v[108:111], v194, v194 op_sel_hi:[0,0,0]
	v_mfma_scale_f32_16x16x128_f8f6f4 v[104:107], v[8:15], v[220:227], v[104:107], v194, v194 op_sel_hi:[0,0,0]
	s_setprio 0
	s_setprio 1
	v_mfma_scale_f32_16x16x128_f8f6f4 v[148:151], v[16:23], v[196:203], v[148:151], v194, v194 op_sel_hi:[0,0,0]
	v_mfma_scale_f32_16x16x128_f8f6f4 v[144:147], v[24:31], v[196:203], v[144:147], v194, v194 op_sel_hi:[0,0,0]
	v_mfma_scale_f32_16x16x128_f8f6f4 v[132:135], v[16:23], v[204:211], v[132:135], v194, v194 op_sel_hi:[0,0,0]
	v_mfma_scale_f32_16x16x128_f8f6f4 v[128:131], v[24:31], v[204:211], v[128:131], v194, v194 op_sel_hi:[0,0,0]
	v_mfma_scale_f32_16x16x128_f8f6f4 v[116:119], v[16:23], v[212:219], v[116:119], v194, v194 op_sel_hi:[0,0,0]
	v_mfma_scale_f32_16x16x128_f8f6f4 v[112:115], v[24:31], v[212:219], v[112:115], v194, v194 op_sel_hi:[0,0,0]
	v_mfma_scale_f32_16x16x128_f8f6f4 v[100:103], v[16:23], v[220:227], v[100:103], v194, v194 op_sel_hi:[0,0,0]
	v_mfma_scale_f32_16x16x128_f8f6f4 v[96:99], v[24:31], v[220:227], v[96:99], v194, v194 op_sel_hi:[0,0,0]
	s_setprio 0
	s_barrier
	s_add_i32 s0, s22, s34
	v_lshl_add_u64 v[178:179], v[178:179], 0, s[10:11]
	s_mov_b32 m0, s0
	ds_read_b128 v[196:199], v193 offset:49152
	global_load_lds_dwordx4 v[178:179], off
	ds_read_b128 v[200:203], v193 offset:50176
	s_add_i32 m0, s0, 0x2000
	s_add_u32 s0, s26, 0xb0080
	v_lshl_add_u64 v[178:179], v[180:181], 0, s[10:11]
	s_addc_u32 s1, s27, 0
	s_add_i32 s22, s23, s34
	global_load_lds_dwordx4 v[178:179], off
	ds_read_b128 v[204:207], v193 offset:51200
	ds_read_b128 v[208:211], v193 offset:52224
	v_lshl_add_u64 v[178:179], s[0:1], 0, v[162:163]
	s_mov_b32 m0, s22
	s_nop 0
	global_load_lds_dwordx4 v[178:179], off
	ds_read_b128 v[212:215], v193 offset:53248
	ds_read_b128 v[216:219], v193 offset:54272
	v_lshl_add_u64 v[178:179], s[0:1], 0, v[166:167]
	s_add_i32 m0, s22, 0x2000
	s_nop 0
	global_load_lds_dwordx4 v[178:179], off
	ds_read_b128 v[220:223], v193 offset:55296
	ds_read_b128 v[224:227], v193 offset:56320
	v_lshl_add_u64 v[178:179], v[182:183], 0, s[10:11]
	s_mov_b32 m0, s69
	s_nop 0
	global_load_lds_dwordx4 v[178:179], off
	v_lshl_add_u64 v[178:179], v[184:185], 0, s[10:11]
	s_mov_b32 m0, s70
	s_nop 0
	global_load_lds_dwordx4 v[178:179], off
	s_waitcnt vmcnt(8)
	s_waitcnt lgkmcnt(0)
	s_barrier
	s_setprio 1
	s_waitcnt lgkmcnt(0)
	v_mfma_scale_f32_16x16x128_f8f6f4 v[92:95], v[0:7], v[196:203], v[92:95], v194, v194 op_sel_hi:[0,0,0]
	v_mfma_scale_f32_16x16x128_f8f6f4 v[88:91], v[8:15], v[196:203], v[88:91], v194, v194 op_sel_hi:[0,0,0]
	v_mfma_scale_f32_16x16x128_f8f6f4 v[76:79], v[0:7], v[204:211], v[76:79], v194, v194 op_sel_hi:[0,0,0]
	v_mfma_scale_f32_16x16x128_f8f6f4 v[72:75], v[8:15], v[204:211], v[72:75], v194, v194 op_sel_hi:[0,0,0]
	v_mfma_scale_f32_16x16x128_f8f6f4 v[60:63], v[0:7], v[212:219], v[60:63], v194, v194 op_sel_hi:[0,0,0]
	v_mfma_scale_f32_16x16x128_f8f6f4 v[56:59], v[8:15], v[212:219], v[56:59], v194, v194 op_sel_hi:[0,0,0]
	v_mfma_scale_f32_16x16x128_f8f6f4 v[44:47], v[0:7], v[220:227], v[44:47], v194, v194 op_sel_hi:[0,0,0]
	v_mfma_scale_f32_16x16x128_f8f6f4 v[40:43], v[8:15], v[220:227], v[40:43], v194, v194 op_sel_hi:[0,0,0]
	s_setprio 0
	s_setprio 1
	v_mfma_scale_f32_16x16x128_f8f6f4 v[84:87], v[16:23], v[196:203], v[84:87], v194, v194 op_sel_hi:[0,0,0]
	v_mfma_scale_f32_16x16x128_f8f6f4 v[80:83], v[24:31], v[196:203], v[80:83], v194, v194 op_sel_hi:[0,0,0]
	v_mfma_scale_f32_16x16x128_f8f6f4 v[68:71], v[16:23], v[204:211], v[68:71], v194, v194 op_sel_hi:[0,0,0]
	v_mfma_scale_f32_16x16x128_f8f6f4 v[64:67], v[24:31], v[204:211], v[64:67], v194, v194 op_sel_hi:[0,0,0]
	v_mfma_scale_f32_16x16x128_f8f6f4 v[52:55], v[16:23], v[212:219], v[52:55], v194, v194 op_sel_hi:[0,0,0]
	v_mfma_scale_f32_16x16x128_f8f6f4 v[48:51], v[24:31], v[212:219], v[48:51], v194, v194 op_sel_hi:[0,0,0]
	v_mfma_scale_f32_16x16x128_f8f6f4 v[36:39], v[16:23], v[220:227], v[36:39], v194, v194 op_sel_hi:[0,0,0]
	v_mfma_scale_f32_16x16x128_f8f6f4 v[32:35], v[24:31], v[220:227], v[32:35], v194, v194 op_sel_hi:[0,0,0]
	s_setprio 0
	s_barrier
	s_add_u32 s31, s31, 0x100
	s_addc_u32 s33, s33, 0
	s_cmp_ge_i32 s36, s30
	s_mov_b64 s[22:23], s[24:25]
	s_mov_b32 s28, s36
	s_cbranch_scc0 .LBB0_2316
	s_nop 15
	s_nop 15
	s_and_b64 vcc, exec, s[54:55]
	s_cbranch_vccz .LBB0_2319
	s_barrier
